# speedup vs baseline: 1.1295x; 1.0416x over previous
.LBB1_6:
	s_or_b64 exec, exec, s[6:7]
	s_ashr_i32 s15, s12, 8
	s_addk_i32 s12, 0xc35
	v_and_b32_e32 v83, 31, v0
	s_load_dwordx2 s[26:27], s[0:1], 0x68
	s_load_dwordx2 s[28:29], s[0:1], 0x30
	s_ashr_i32 s33, s12, 8
	v_lshlrev_b32_e32 v82, 3, v83
	s_movk_i32 s37, 0x110
	s_sub_i32 s34, s33, s15
	v_mad_u32_u24 v144, v155, s37, v82
	s_waitcnt vmcnt(22)
	v_cvt_pk_f16_f32 v85, v4, v5
	v_cvt_pk_f16_f32 v84, v2, v3
	s_add_i32 s4, s34, 3
	ds_write_b64 v144, v[84:85]
	s_waitcnt vmcnt(21)
	v_cvt_pk_f16_f32 v85, v8, v9
	v_cvt_pk_f16_f32 v84, v6, v7
	s_and_b32 s5, s2, 7
	ds_write_b64 v144, v[84:85] offset:4352
	s_waitcnt vmcnt(20)
	v_cvt_pk_f16_f32 v85, v76, v77
	v_cvt_pk_f16_f32 v84, v74, v75
	s_ashr_i32 s35, s4, 2
	ds_write_b64 v144, v[84:85] offset:8704
	s_waitcnt vmcnt(19)
	v_cvt_pk_f16_f32 v85, v80, v81
	v_cvt_pk_f16_f32 v84, v78, v79
	v_bfe_u32 v143, v0, 4, 2
	v_cmp_eq_u32_e64 s[12:13], s5, v1
	s_cmp_lt_i32 s35, 1
	v_lshlrev_b32_e32 v142, 2, v0
	ds_write_b64 v144, v[84:85] offset:13056
	s_waitcnt lgkmcnt(0)
	s_barrier
	s_cbranch_scc1 .LBB1_58
	s_load_dwordx2 s[10:11], s[0:1], 0x60
	s_load_dwordx8 s[16:23], s[0:1], 0x38
	s_load_dwordx4 s[4:7], s[0:1], 0x18
	s_load_dwordx2 s[30:31], s[0:1], 0x28
	s_movk_i32 s0, 0x17f
	v_mov_b32_e32 v85, 0x3f800008
	v_cmp_lt_u32_e32 vcc, s0, v0
	s_movk_i32 s0, 0x13f
	s_addk_i32 s2, 0x7f
	v_cndmask_b32_e32 v82, 0, v85, vcc
	v_cmp_lt_u32_e32 vcc, s0, v0
	s_mul_i32 s0, s3, 0x186a
	s_ashr_i32 s1, s0, 31
	s_lshl_b64 s[0:1], s[0:1], 2
	s_cmpk_lt_u32 s2, 0xff
	s_waitcnt lgkmcnt(0)
	s_cselect_b32 s18, s18, s22
	v_cndmask_b32_e32 v85, 0, v85, vcc
	s_cselect_b32 s2, s19, s23
	s_cselect_b32 s19, s17, s21
	s_cselect_b32 s20, s16, s20
	s_add_u32 s16, s18, s0
	s_waitcnt vmcnt(1)
	v_mul_f32_e32 v86, v85, v151
	s_waitcnt vmcnt(0)
	v_mul_f32_e32 v90, v85, v152
	s_addc_u32 s17, s2, s1
	v_min_u32_e32 v85, 0x69, v0
	v_mov_b32_e32 v87, 0x6000
	v_lshl_or_b32 v85, v85, 2, v87
	s_add_u32 s0, s20, s0
	s_addc_u32 s1, s19, s1
	global_load_dword v115, v85, s[16:17]
	global_load_dword v94, v85, s[0:1]
	v_or_b32_e32 v85, 0x5800, v142
	global_load_dword v95, v85, s[16:17]
	global_load_dword v96, v85, s[0:1]
	v_or_b32_e32 v85, 0x5000, v142
	global_load_dword v97, v85, s[16:17]
	global_load_dword v98, v85, s[0:1]
	v_or_b32_e32 v85, 0x4800, v142
	global_load_dword v99, v85, s[16:17]
	global_load_dword v100, v85, s[0:1]
	v_or_b32_e32 v85, 0x4000, v142
	global_load_dword v101, v85, s[16:17]
	global_load_dword v102, v85, s[0:1]
	v_or_b32_e32 v85, 0x3800, v142
	global_load_dword v103, v85, s[16:17]
	global_load_dword v104, v85, s[0:1]
	v_or_b32_e32 v85, 0x3000, v142
	v_or_b32_e32 v87, 0xa00, v0
	global_load_dword v105, v85, s[16:17]
	global_load_dword v106, v85, s[0:1]
	v_lshlrev_b32_e32 v85, 2, v87
	global_load_dword v107, v85, s[16:17]
	global_load_dword v108, v85, s[0:1]
	v_or_b32_e32 v85, 0x2000, v142
	global_load_dword v109, v85, s[16:17]
	global_load_dword v110, v85, s[0:1]
	global_load_dword v112, v142, s[0:1]
	v_or_b32_e32 v88, 0x600, v0
	v_lshlrev_b32_e32 v85, 2, v88
	global_load_dword v111, v85, s[16:17]
	global_load_dword v114, v85, s[0:1]
	v_or_b32_e32 v85, 0x1000, v142
	global_load_dword v117, v85, s[16:17]
	global_load_dword v116, v85, s[0:1]
	global_load_dword v119, v142, s[16:17] offset:2048
	global_load_dword v118, v142, s[0:1] offset:2048
	global_load_dword v122, v142, s[16:17]
	v_lshlrev_b32_e32 v84, 3, v0
	s_add_u32 s0, s4, 0xc35000
	v_lshlrev_b32_e32 v126, 4, v83
	v_mov_b32_e32 v127, 0
	s_movk_i32 s2, 0x200
	s_addc_u32 s1, s5, 0
	v_lshl_add_u64 v[128:129], s[24:25], 0, v[126:127]
	v_and_b32_e32 v83, 0x78, v84
	v_lshlrev_b32_e32 v126, 2, v142
	v_or_b32_e32 v85, 0x200, v0
	v_lshl_add_u64 v[130:131], s[30:31], 0, v[126:127]
	v_add_u32_e32 v152, 0x15400, v126
	v_lshlrev_b32_e32 v126, 1, v83
	v_and_b32_e32 v228, 0x10, v126
	v_and_b32_e32 v229, 0x60, v126
	v_lshrrev_b32_e32 v229, 1, v229
	v_lshl_add_u32 v229, v228, 2, v229
	v_lshrrev_b32_e32 v228, 7, v126
	v_mul_u32_u24_e32 v228, 0x61a800, v228
	v_add_u32_e32 v228, v228, v229
	v_mov_b32_e32 v229, 0
	v_mov_b32_e32 v83, s1
	v_mov_b32_e32 v84, s5
	v_cmp_gt_u32_e32 vcc, s2, v0
	v_lshrrev_b32_e32 v157, 4, v85
	v_bfe_u32 v159, v88, 4, 6
	v_cndmask_b32_e32 v85, v83, v84, vcc
	v_mov_b32_e32 v83, s0
	v_mov_b32_e32 v84, s4
	v_cndmask_b32_e32 v84, v83, v84, vcc
	v_lshl_add_u64 v[136:137], s[0:1], 0, v[228:229]
	v_mul_u32_u24_e32 v83, 0x330, v159
	s_movk_i32 s0, 0x100
	v_bfe_u32 v161, v87, 4, 6
	v_lshrrev_b32_e32 v145, 4, v0
	s_movk_i32 s16, 0x330
	v_add3_u32 v160, v83, v126, s0
	v_mul_u32_u24_e32 v83, 0x330, v161
	s_mul_i32 s0, s14, 0x101
	v_mad_u32_u24 v156, v145, s16, v126
	v_lshl_add_u64 v[132:133], s[4:5], 0, v[228:229]
	v_mad_u32_u24 v158, v157, s16, v126
	v_lshl_add_u64 v[134:135], v[84:85], 0, v[228:229]
	v_lshl_add_u64 v[138:139], s[6:7], 0, v[228:229]
	v_add3_u32 v126, v83, v126, s2
	s_cmp_eq_u32 s3, 0
	v_add_u32_e32 v120, s0, v0
	s_mov_b32 s2, 0x5397829d
	s_cselect_b64 s[16:17], -1, 0
	v_ashrrev_i32_e32 v121, 31, v120
	s_ashr_i32 s1, s0, 31
	v_lshl_add_u64 v[140:141], v[120:121], 2, s[10:11]
	s_lshl_b64 s[0:1], s[0:1], 2
	s_add_u32 s18, s10, s0
	s_movk_i32 s3, 0xff3c
	s_addc_u32 s19, s11, s1
	s_mov_b32 s20, 0xff9e
	v_mul_i32_i24_e32 v123, 0xfffffef2, v146
	v_mul_u32_u24_e32 v125, 0x60, v1
	v_mul_f32_e32 v82, v82, v153
	s_movk_i32 s38, 0xff
	v_lshlrev_b32_e32 v124, 4, v143
	s_mov_b32 s36, 0
	v_or_b32_e32 v150, 64, v155
	v_lshrrev_b32_e32 v151, 2, v0
	v_or_b32_e32 v153, 0x50, v155
	v_or_b32_e32 v154, 0x60, v155
	v_or_b32_e32 v155, 0x70, v155
	v_mov_b32_e32 v83, v82
	v_mov_b32_e32 v84, v82
	v_mov_b32_e32 v85, v82
	v_mov_b32_e32 v87, v86
	v_mov_b32_e32 v88, v86
	v_mov_b32_e32 v89, v86
	v_mov_b32_e32 v91, v90
	v_mov_b32_e32 v92, v90
	v_mov_b32_e32 v93, v90
	v_cmp_lt_u32_e64 s[4:5], 63, v0
	v_sub_u32_e32 v162, v149, v162
	v_sub_u32_e32 v163, v163, v164
	v_add_u32_e32 v164, 0x22b80, v142
	s_waitcnt vmcnt(7)
	v_mul_hi_i32 v113, v112, s2
	v_lshrrev_b32_e32 v120, 31, v113
	v_ashrrev_i32_e32 v113, 6, v113
	v_add_u32_e32 v120, v113, v120
	v_mad_u64_u32 v[112:113], s[0:1], v120, s3, v[112:113]
	v_mul_hi_i32 v113, v112, s2
	v_lshrrev_b32_e32 v121, 31, v113
	v_ashrrev_i32_e32 v113, 5, v113
	v_add_u32_e32 v113, v113, v121
	v_lshlrev_b32_e32 v121, 23, v113
	v_mul_lo_u32 v113, v113, s20
	v_add_lshl_u32 v112, v113, v112, 16
	s_waitcnt vmcnt(0)
	v_or3_b32 v168, v121, v122, v112
	v_mul_hi_i32 v112, v118, s2
	v_lshlrev_b32_e32 v120, 2, v120
	v_lshrrev_b32_e32 v113, 31, v112
	v_ashrrev_i32_e32 v112, 6, v112
	v_add_u32_e32 v167, 0x22780, v120
	v_add_u32_e32 v169, 0x22b80, v120
	v_add_u32_e32 v170, 0x22f80, v120
	v_add_u32_e32 v120, v112, v113
	v_mad_u64_u32 v[112:113], s[0:1], v120, s3, v[118:119]
	v_mul_hi_i32 v113, v112, s2
	v_lshrrev_b32_e32 v118, 31, v113
	v_ashrrev_i32_e32 v113, 5, v113
	v_add_u32_e32 v113, v113, v118
	v_lshlrev_b32_e32 v118, 2, v120
	v_lshlrev_b32_e32 v120, 23, v113
	v_mul_lo_u32 v113, v113, s20
	v_add_lshl_u32 v112, v113, v112, 16
	v_or3_b32 v172, v120, v119, v112
	v_mul_hi_i32 v112, v116, s2
	v_lshrrev_b32_e32 v113, 31, v112
	v_ashrrev_i32_e32 v112, 6, v112
	v_add_u32_e32 v171, 0x22780, v118
	v_add_u32_e32 v173, 0x22b80, v118
	v_add_u32_e32 v174, 0x22f80, v118
	v_add_u32_e32 v118, v112, v113
	v_mad_u64_u32 v[112:113], s[0:1], v118, s3, v[116:117]
	v_mul_hi_i32 v113, v112, s2
	v_lshrrev_b32_e32 v116, 31, v113
	v_ashrrev_i32_e32 v113, 5, v113
	v_add_u32_e32 v113, v113, v116
	v_lshlrev_b32_e32 v116, 2, v118
	v_lshlrev_b32_e32 v118, 23, v113
	v_mul_lo_u32 v113, v113, s20
	v_add_lshl_u32 v112, v113, v112, 16
	v_or3_b32 v176, v118, v117, v112
	v_mul_hi_i32 v112, v114, s2
	v_lshrrev_b32_e32 v113, 31, v112
	v_ashrrev_i32_e32 v112, 6, v112
	v_add_u32_e32 v175, 0x22780, v116
	v_add_u32_e32 v177, 0x22b80, v116
	v_add_u32_e32 v178, 0x22f80, v116
	v_add_u32_e32 v116, v112, v113
	v_mad_u64_u32 v[112:113], s[0:1], v116, s3, v[114:115]
	v_mul_hi_i32 v113, v112, s2
	v_lshrrev_b32_e32 v114, 31, v113
	v_ashrrev_i32_e32 v113, 5, v113
	v_add_u32_e32 v113, v113, v114
	v_lshlrev_b32_e32 v114, 2, v116
	v_lshlrev_b32_e32 v116, 23, v113
	v_mul_lo_u32 v113, v113, s20
	v_add_lshl_u32 v112, v113, v112, 16
	v_or3_b32 v180, v116, v111, v112
	v_mul_hi_i32 v111, v110, s2
	v_lshrrev_b32_e32 v112, 31, v111
	v_ashrrev_i32_e32 v111, 6, v111
	v_add_u32_e32 v112, v111, v112
	v_mad_u64_u32 v[110:111], s[0:1], v112, s3, v[110:111]
	v_mul_hi_i32 v111, v110, s2
	v_lshrrev_b32_e32 v113, 31, v111
	v_ashrrev_i32_e32 v111, 5, v111
	v_add_u32_e32 v111, v111, v113
	v_lshlrev_b32_e32 v113, 23, v111
	v_mul_lo_u32 v111, v111, s20
	v_add_lshl_u32 v110, v111, v110, 16
	v_or3_b32 v184, v113, v109, v110
	v_mul_hi_i32 v109, v108, s2
	v_lshrrev_b32_e32 v110, 31, v109
	v_ashrrev_i32_e32 v109, 6, v109
	v_add_u32_e32 v110, v109, v110
	v_mad_u64_u32 v[108:109], s[0:1], v110, s3, v[108:109]
	v_mul_hi_i32 v109, v108, s2
	v_lshrrev_b32_e32 v111, 31, v109
	v_ashrrev_i32_e32 v109, 5, v109
	v_add_u32_e32 v109, v109, v111
	v_lshlrev_b32_e32 v111, 23, v109
	v_mul_lo_u32 v109, v109, s20
	v_add_lshl_u32 v108, v109, v108, 16
	v_or3_b32 v188, v111, v107, v108
	v_mul_hi_i32 v107, v106, s2
	v_lshrrev_b32_e32 v108, 31, v107
	v_ashrrev_i32_e32 v107, 6, v107
	v_add_u32_e32 v108, v107, v108
	v_mad_u64_u32 v[106:107], s[0:1], v108, s3, v[106:107]
	v_mul_hi_i32 v107, v106, s2
	v_lshrrev_b32_e32 v109, 31, v107
	v_ashrrev_i32_e32 v107, 5, v107
	v_add_u32_e32 v107, v107, v109
	v_lshlrev_b32_e32 v109, 23, v107
	v_mul_lo_u32 v107, v107, s20
	v_add_lshl_u32 v106, v107, v106, 16
	v_or3_b32 v192, v109, v105, v106
	v_mul_hi_i32 v105, v104, s2
	v_lshrrev_b32_e32 v106, 31, v105
	v_ashrrev_i32_e32 v105, 6, v105
	v_add_u32_e32 v106, v105, v106
	v_mad_u64_u32 v[104:105], s[0:1], v106, s3, v[104:105]
	v_mul_hi_i32 v105, v104, s2
	v_lshrrev_b32_e32 v107, 31, v105
	v_ashrrev_i32_e32 v105, 5, v105
	v_add_u32_e32 v105, v105, v107
	v_lshlrev_b32_e32 v107, 23, v105
	v_mul_lo_u32 v105, v105, s20
	v_add_lshl_u32 v104, v105, v104, 16
	v_or3_b32 v196, v107, v103, v104
	v_mul_hi_i32 v103, v102, s2
	v_lshrrev_b32_e32 v104, 31, v103
	v_ashrrev_i32_e32 v103, 6, v103
	v_add_u32_e32 v104, v103, v104
	v_mad_u64_u32 v[102:103], s[0:1], v104, s3, v[102:103]
	v_mul_hi_i32 v103, v102, s2
	v_lshrrev_b32_e32 v105, 31, v103
	v_ashrrev_i32_e32 v103, 5, v103
	v_add_u32_e32 v103, v103, v105
	v_lshlrev_b32_e32 v105, 23, v103
	v_mul_lo_u32 v103, v103, s20
	v_add_lshl_u32 v102, v103, v102, 16
	v_or3_b32 v200, v105, v101, v102
	v_mul_hi_i32 v101, v100, s2
	v_lshrrev_b32_e32 v102, 31, v101
	v_ashrrev_i32_e32 v101, 6, v101
	v_add_u32_e32 v102, v101, v102
	v_mad_u64_u32 v[100:101], s[0:1], v102, s3, v[100:101]
	v_mul_hi_i32 v101, v100, s2
	v_lshrrev_b32_e32 v103, 31, v101
	v_ashrrev_i32_e32 v101, 5, v101
	v_add_u32_e32 v101, v101, v103
	v_lshlrev_b32_e32 v103, 23, v101
	v_mul_lo_u32 v101, v101, s20
	v_add_lshl_u32 v100, v101, v100, 16
	v_or3_b32 v204, v103, v99, v100
	v_mul_hi_i32 v99, v98, s2
	v_lshrrev_b32_e32 v100, 31, v99
	v_ashrrev_i32_e32 v99, 6, v99
	v_add_u32_e32 v100, v99, v100
	v_mad_u64_u32 v[98:99], s[0:1], v100, s3, v[98:99]
	v_mul_hi_i32 v99, v98, s2
	v_lshrrev_b32_e32 v101, 31, v99
	v_ashrrev_i32_e32 v99, 5, v99
	v_add_u32_e32 v99, v99, v101
	v_lshlrev_b32_e32 v101, 23, v99
	v_mul_lo_u32 v99, v99, s20
	v_add_lshl_u32 v98, v99, v98, 16
	v_or3_b32 v208, v101, v97, v98
	v_mul_hi_i32 v97, v96, s2
	v_lshrrev_b32_e32 v98, 31, v97
	v_ashrrev_i32_e32 v97, 6, v97
	v_add_u32_e32 v98, v97, v98
	v_mad_u64_u32 v[96:97], s[10:11], v98, s3, v[96:97]
	v_mul_hi_i32 v97, v96, s2
	v_lshrrev_b32_e32 v99, 31, v97
	v_ashrrev_i32_e32 v97, 5, v97
	v_add_u32_e32 v97, v97, v99
	v_lshlrev_b32_e32 v99, 23, v97
	v_mul_lo_u32 v97, v97, s20
	v_add_lshl_u32 v96, v97, v96, 16
	v_or3_b32 v212, v99, v95, v96
	v_mul_hi_i32 v95, v94, s2
	v_lshrrev_b32_e32 v96, 31, v95
	v_ashrrev_i32_e32 v95, 6, v95
	v_add_u32_e32 v96, v95, v96
	v_mad_u64_u32 v[94:95], s[22:23], v96, s3, v[94:95]
	v_mul_hi_i32 v95, v94, s2
	v_lshrrev_b32_e32 v97, 31, v95
	v_ashrrev_i32_e32 v95, 5, v95
	v_add_u32_e32 v95, v95, v97
	v_lshlrev_b32_e32 v97, 23, v95
	v_mul_lo_u32 v95, v95, s20
	v_add_lshl_u32 v94, v95, v94, 16
	v_or3_b32 v217, v97, v115, v94
	v_lshlrev_b32_e32 v94, 2, v146
	v_lshl_or_b32 v220, v143, 8, v94
	v_mul_u32_u24_e32 v94, 0xcc0, v143
	v_lshlrev_b32_e32 v112, 2, v112
	v_lshlrev_b32_e32 v110, 2, v110
	v_lshlrev_b32_e32 v108, 2, v108
	v_lshlrev_b32_e32 v106, 2, v106
	v_lshlrev_b32_e32 v104, 2, v104
	v_lshlrev_b32_e32 v102, 2, v102
	v_lshlrev_b32_e32 v100, 2, v100
	s_movk_i32 s0, 0x26a
	v_lshlrev_b32_e32 v98, 2, v98
	s_movk_i32 s10, 0x6a
	v_lshlrev_b32_e32 v96, 2, v96
	v_add3_u32 v94, v123, v125, v94
	v_mul_u32_u24_e32 v95, 0x110, v146
	s_mov_b32 s2, 0x8800
	v_add_u32_e32 v165, 0x22f80, v142
	v_add_u32_e32 v166, 0x22780, v142
	v_cmp_eq_u32_e64 s[6:7], s38, v0
	v_add_u32_e32 v179, 0x22780, v114
	v_add_u32_e32 v181, 0x22b80, v114
	v_add_u32_e32 v182, 0x22f80, v114
	v_add_u32_e32 v183, 0x22780, v112
	v_add_u32_e32 v185, 0x22b80, v112
	v_add_u32_e32 v186, 0x22f80, v112
	v_add_u32_e32 v187, 0x22780, v110
	v_add_u32_e32 v189, 0x22b80, v110
	v_add_u32_e32 v190, 0x22f80, v110
	v_add_u32_e32 v191, 0x22780, v108
	v_add_u32_e32 v193, 0x22b80, v108
	v_add_u32_e32 v194, 0x22f80, v108
	v_add_u32_e32 v195, 0x22780, v106
	v_add_u32_e32 v197, 0x22b80, v106
	v_add_u32_e32 v198, 0x22f80, v106
	v_add_u32_e32 v199, 0x22780, v104
	v_add_u32_e32 v201, 0x22b80, v104
	v_add_u32_e32 v202, 0x22f80, v104
	v_add_u32_e32 v203, 0x22780, v102
	v_add_u32_e32 v205, 0x22b80, v102
	v_add_u32_e32 v206, 0x22f80, v102
	v_add_u32_e32 v207, 0x22780, v100
	v_add_u32_e32 v209, 0x22b80, v100
	v_add_u32_e32 v210, 0x22f80, v100
	v_cmp_gt_u32_e64 s[0:1], s0, v0
	v_add_u32_e32 v211, 0x22780, v98
	v_add_u32_e32 v213, 0x22b80, v98
	v_add_u32_e32 v214, 0x22f80, v98
	v_cmp_gt_u32_e64 s[10:11], s10, v0
	v_add_u32_e32 v216, 0x22780, v96
	v_add_u32_e32 v218, 0x22b80, v96
	v_add_u32_e32 v219, 0x22f80, v96
	v_add3_u32 v221, v94, v95, s2
	v_mad_u32_u24 v222, v146, s37, v124
	v_mov_b32_e32 v215, 0xff800000
	s_mov_b64 s[20:21], 0
	s_movk_i32 s37, 0x4400
	v_mov_b32_e32 v223, 1

_Z10agg_kernelPKjPKiPKDF16_S4_PKfS4_S0_S2_S2_S2_S2_Pf:
	s_and_b32 s3, s2, 1
	s_lshr_b32 s4, s2, 1
	s_load_dwordx16 s[8:23], s[0:1], 0x0
	s_load_dwordx8 s[24:31], s[0:1], 0x40
	s_mul_i32 s6, s4, 0xc4
	s_sub_u32 s5, 0xc350, s6
	s_min_u32 s5, s5, 0xc4
	v_lshrrev_b32_e32 v2, 2, v0
	v_and_b32_e32 v1, 3, v0
	v_lshrrev_b32_e32 v13, 1, v1
	v_lshl_add_u32 v13, s3, 1, v13
	v_lshlrev_b32_e32 v13, 2, v13
	v_lshlrev_b32_e32 v1, 4, v1
	s_lshl_b32 s52, s4, 2
	s_waitcnt lgkmcnt(0)
	s_add_u32 s52, s10, s52
	s_addc_u32 s53, s11, 0
	s_load_dwordx2 s[32:33], s[52:53], 0x0
	s_load_dwordx2 s[36:37], s[52:53], 0x404
	v_add_u32_e32 v40, s6, v2
	v_min_u32_e32 v40, 0xc34f, v40
	v_lshlrev_b32_e32 v40, 6, v40
	v_add3_u32 v40, v40, v13, 16
	global_load_dword v3, v40, s[16:17]
	global_load_dword v4, v40, s[16:17] offset:32
	v_lshlrev_b32_e32 v62, 2, v0
	v_mov_b32_e32 v63, 0
	ds_write_b32 v62, v63 offset:21248
	v_cmp_gt_u32_e32 vcc, 0x80, v0
	s_and_saveexec_b64 s[60:61], vcc
	ds_write_b32 v62, v63 offset:20032
	s_mov_b64 exec, s[60:61]
	s_waitcnt lgkmcnt(0)
	s_sub_u32 s38, s33, s32
	s_sub_u32 s39, s37, s36
	s_lshl_b32 s52, s32, 2
	s_add_u32 s42, s8, s52
	s_addc_u32 s43, s9, 0
	s_add_u32 s52, s36, 0xc3500
	s_lshl_b32 s52, s52, 2
	s_add_u32 s44, s8, s52
	s_addc_u32 s45, s9, 0
	s_max_i32 s52, s38, 1
	s_sub_u32 s52, s52, 1
	s_max_i32 s53, s39, 1
	s_sub_u32 s53, s53, 1
	s_movk_i32 s46, 0x80
	s_movk_i32 s55, 0x62
	s_movk_i32 s47, 0x61a8
	v_min_u32_e32 v41, s52, v0
	v_lshlrev_b32_e32 v41, 2, v41
	global_load_dword v8, v41, s[42:43]
	v_min_u32_e32 v41, s53, v0
	v_lshlrev_b32_e32 v41, 2, v41
	global_load_dword v24, v41, s[44:45]
	v_add_u32_e32 v40, 0x400, v0
	v_min_u32_e32 v41, s52, v40
	v_lshlrev_b32_e32 v41, 2, v41
	global_load_dword v9, v41, s[42:43]
	v_min_u32_e32 v41, s53, v40
	v_lshlrev_b32_e32 v41, 2, v41
	global_load_dword v25, v41, s[44:45]
	v_add_u32_e32 v40, 0x800, v0
	v_min_u32_e32 v41, s52, v40
	v_lshlrev_b32_e32 v41, 2, v41
	global_load_dword v10, v41, s[42:43]
	v_min_u32_e32 v41, s53, v40
	v_lshlrev_b32_e32 v41, 2, v41
	global_load_dword v26, v41, s[44:45]
	v_add_u32_e32 v40, 0xc00, v0
	v_min_u32_e32 v41, s52, v40
	v_lshlrev_b32_e32 v41, 2, v41
	global_load_dword v11, v41, s[42:43]
	v_min_u32_e32 v41, s53, v40
	v_lshlrev_b32_e32 v41, 2, v41
	global_load_dword v27, v41, s[44:45]
	v_mov_b32_e32 v61, 1
	v_mov_b32_e32 v43, 0xc4
	s_barrier
	s_waitcnt vmcnt(7)
	v_bfe_u32 v41, v8, 16, 7
	v_bfe_u32 v42, v8, 23, 1
	v_and_b32_e32 v44, 0xffff, v8
	v_mad_u32_u24 v41, v42, s55, v41
	v_cmp_le_u32_e32 vcc, s47, v44
	v_lshlrev_b32_e32 v41, 2, v41
	s_nop 0
	v_cndmask_b32_e32 v42, 0, v43, vcc
	v_lshl_add_u32 v41, v42, 2, v41
	v_cmp_gt_u32_e32 vcc, s38, v0
	s_and_saveexec_b64 s[60:61], vcc
	ds_add_rtn_u32 v16, v41, v61 offset:21248
	s_mov_b64 exec, s[60:61]
	s_waitcnt vmcnt(6)
	v_bfe_u32 v41, v24, 16, 7
	v_bfe_u32 v42, v24, 23, 1
	v_and_b32_e32 v44, 0xffff, v24
	v_mad_u32_u24 v41, v42, s55, v41
	v_cmp_le_u32_e32 vcc, s47, v44
	v_lshlrev_b32_e32 v41, 2, v41
	s_nop 0
	v_cndmask_b32_e32 v42, 0, v43, vcc
	v_lshl_add_u32 v41, v42, 2, v41
	v_cmp_gt_u32_e32 vcc, s39, v0
	s_and_saveexec_b64 s[60:61], vcc
	ds_add_rtn_u32 v20, v41, v61 offset:23296
	s_mov_b64 exec, s[60:61]
	s_waitcnt vmcnt(5)
	v_add_u32_e32 v40, 0x400, v0
	v_bfe_u32 v41, v9, 16, 7
	v_bfe_u32 v42, v9, 23, 1
	v_and_b32_e32 v44, 0xffff, v9
	v_mad_u32_u24 v41, v42, s55, v41
	v_cmp_le_u32_e32 vcc, s47, v44
	v_lshlrev_b32_e32 v41, 2, v41
	s_nop 0
	v_cndmask_b32_e32 v42, 0, v43, vcc
	v_lshl_add_u32 v41, v42, 2, v41
	v_cmp_gt_u32_e32 vcc, s38, v40
	s_and_saveexec_b64 s[60:61], vcc
	ds_add_rtn_u32 v17, v41, v61 offset:21248
	s_mov_b64 exec, s[60:61]
	s_waitcnt vmcnt(4)
	v_bfe_u32 v41, v25, 16, 7
	v_bfe_u32 v42, v25, 23, 1
	v_and_b32_e32 v44, 0xffff, v25
	v_mad_u32_u24 v41, v42, s55, v41
	v_cmp_le_u32_e32 vcc, s47, v44
	v_lshlrev_b32_e32 v41, 2, v41
	s_nop 0
	v_cndmask_b32_e32 v42, 0, v43, vcc
	v_lshl_add_u32 v41, v42, 2, v41
	v_cmp_gt_u32_e32 vcc, s39, v40
	s_and_saveexec_b64 s[60:61], vcc
	ds_add_rtn_u32 v21, v41, v61 offset:23296
	s_mov_b64 exec, s[60:61]
	s_waitcnt vmcnt(3)
	v_add_u32_e32 v40, 0x800, v0
	v_bfe_u32 v41, v10, 16, 7
	v_bfe_u32 v42, v10, 23, 1
	v_and_b32_e32 v44, 0xffff, v10
	v_mad_u32_u24 v41, v42, s55, v41
	v_cmp_le_u32_e32 vcc, s47, v44
	v_lshlrev_b32_e32 v41, 2, v41
	s_nop 0
	v_cndmask_b32_e32 v42, 0, v43, vcc
	v_lshl_add_u32 v41, v42, 2, v41
	v_cmp_gt_u32_e32 vcc, s38, v40
	s_and_saveexec_b64 s[60:61], vcc
	ds_add_rtn_u32 v18, v41, v61 offset:21248
	s_mov_b64 exec, s[60:61]
	s_waitcnt vmcnt(2)
	v_bfe_u32 v41, v26, 16, 7
	v_bfe_u32 v42, v26, 23, 1
	v_and_b32_e32 v44, 0xffff, v26
	v_mad_u32_u24 v41, v42, s55, v41
	v_cmp_le_u32_e32 vcc, s47, v44
	v_lshlrev_b32_e32 v41, 2, v41
	s_nop 0
	v_cndmask_b32_e32 v42, 0, v43, vcc
	v_lshl_add_u32 v41, v42, 2, v41
	v_cmp_gt_u32_e32 vcc, s39, v40
	s_and_saveexec_b64 s[60:61], vcc
	ds_add_rtn_u32 v22, v41, v61 offset:23296
	s_mov_b64 exec, s[60:61]
	s_waitcnt vmcnt(1)
	v_add_u32_e32 v40, 0xc00, v0
	v_bfe_u32 v41, v11, 16, 7
	v_bfe_u32 v42, v11, 23, 1
	v_and_b32_e32 v44, 0xffff, v11
	v_mad_u32_u24 v41, v42, s55, v41
	v_cmp_le_u32_e32 vcc, s47, v44
	v_lshlrev_b32_e32 v41, 2, v41
	s_nop 0
	v_cndmask_b32_e32 v42, 0, v43, vcc
	v_lshl_add_u32 v41, v42, 2, v41
	v_cmp_gt_u32_e32 vcc, s38, v40
	s_and_saveexec_b64 s[60:61], vcc
	ds_add_rtn_u32 v19, v41, v61 offset:21248
	s_mov_b64 exec, s[60:61]
	s_waitcnt vmcnt(0)
	v_bfe_u32 v41, v27, 16, 7
	v_bfe_u32 v42, v27, 23, 1
	v_and_b32_e32 v44, 0xffff, v27
	v_mad_u32_u24 v41, v42, s55, v41
	v_cmp_le_u32_e32 vcc, s47, v44
	v_lshlrev_b32_e32 v41, 2, v41
	s_nop 0
	v_cndmask_b32_e32 v42, 0, v43, vcc
	v_lshl_add_u32 v41, v42, 2, v41
	v_cmp_gt_u32_e32 vcc, s39, v40
	s_and_saveexec_b64 s[60:61], vcc
	ds_add_rtn_u32 v23, v41, v61 offset:23296
	s_mov_b64 exec, s[60:61]
	s_waitcnt lgkmcnt(0)
	s_barrier
	ds_read_b32 v40, v62 offset:21248
	v_and_b32_e32 v44, 63, v0
	v_lshrrev_b32_e32 v45, 6, v0
	v_lshlrev_b32_e32 v45, 2, v45
	v_and_b32_e32 v52, 0x1ff, v0
	v_lshrrev_b32_e32 v51, 9, v0
	v_cmp_le_u32_e32 vcc, 0xc4, v52
	v_mov_b32_e32 v47, 31
	s_nop 0
	v_cndmask_b32_e64 v53, 0, 1, vcc
	v_mul_u32_u24_e32 v54, 0xc4, v53
	v_sub_u32_e32 v54, v52, v54
	v_lshl_add_u32 v53, v51, 1, v53
	s_waitcnt lgkmcnt(0)
	v_min_u32_e32 v55, 31, v40
	v_sub_u32_e32 v55, v47, v55
	v_lshl_add_u32 v55, v53, 5, v55
	v_lshlrev_b32_e32 v55, 2, v55
	v_cmp_gt_u32_e32 vcc, 0x188, v52
	s_and_saveexec_b64 s[60:61], vcc
	ds_add_rtn_u32 v51, v55, v61 offset:20032
	s_mov_b64 exec, s[60:61]
	v_mov_b32_e32 v41, v40
	s_nop 1
	v_add_u32_dpp v41, v41, v41 row_shr:1 row_mask:0xf bank_mask:0xf
	s_nop 1
	v_add_u32_dpp v41, v41, v41 row_shr:2 row_mask:0xf bank_mask:0xf
	s_nop 1
	v_add_u32_dpp v41, v41, v41 row_shr:4 row_mask:0xf bank_mask:0xf
	s_nop 1
	v_add_u32_dpp v41, v41, v41 row_shr:8 row_mask:0xf bank_mask:0xf
	s_nop 1
	v_add_u32_dpp v41, v41, v41 row_bcast:15 row_mask:0xa bank_mask:0xf
	s_nop 1
	v_add_u32_dpp v41, v41, v41 row_bcast:31 row_mask:0xc bank_mask:0xf
	v_cmp_eq_u32_e32 vcc, 63, v44
	s_and_saveexec_b64 s[60:61], vcc
	ds_write_b32 v45, v41 offset:21056
	s_mov_b64 exec, s[60:61]
	s_waitcnt lgkmcnt(0)
	s_barrier
	v_cmp_gt_u32_e32 vcc, 0x80, v0
	s_and_saveexec_b64 s[60:61], vcc
	s_cbranch_execz .Lagg_bins_done
	ds_read_b32 v48, v62 offset:20032
	s_waitcnt lgkmcnt(0)
	v_mov_b32_e32 v49, v48
	s_nop 1
	v_add_u32_dpp v49, v49, v49 row_shr:1 row_mask:0xf bank_mask:0xf
	s_nop 1
	v_add_u32_dpp v49, v49, v49 row_shr:2 row_mask:0xf bank_mask:0xf
	s_nop 1
	v_add_u32_dpp v49, v49, v49 row_shr:4 row_mask:0xf bank_mask:0xf
	s_nop 1
	v_add_u32_dpp v49, v49, v49 row_shr:8 row_mask:0xf bank_mask:0xf
	s_nop 1
	v_add_u32_dpp v49, v49, v49 row_bcast:15 row_mask:0xa bank_mask:0xf
	s_nop 0
	v_sub_u32_e32 v50, v49, v48
	ds_write_b32 v62, v50 offset:20544
.Lagg_bins_done:
	s_mov_b64 exec, s[60:61]
	v_cmp_gt_u32_e32 vcc, 64, v0
	s_and_saveexec_b64 s[60:61], vcc
	s_cbranch_execz .Lagg_w0_done
	v_and_b32_e32 v46, 7, v0
	v_lshrrev_b32_e32 v47, 4, v0
	v_lshl_add_u32 v46, v47, 3, v46
	v_lshlrev_b32_e32 v46, 2, v46
	v_and_b32_e32 v47, 0x28, v0
	v_mov_b32_e32 v48, 0
	v_cmp_eq_u32_e32 vcc, 0, v47
	s_and_saveexec_b64 s[62:63], vcc
	ds_read_b32 v48, v46 offset:21056
	s_waitcnt lgkmcnt(0)
	s_mov_b64 exec, s[62:63]
	v_mov_b32_e32 v49, v48
	s_nop 1
	v_add_u32_dpp v49, v49, v49 row_shr:1 row_mask:0xf bank_mask:0xf
	s_nop 1
	v_add_u32_dpp v49, v49, v49 row_shr:2 row_mask:0xf bank_mask:0xf
	s_nop 1
	v_add_u32_dpp v49, v49, v49 row_shr:4 row_mask:0xf bank_mask:0xf
	s_nop 1
	v_sub_u32_e32 v50, v49, v48
	s_and_b64 exec, exec, vcc
	ds_write_b32 v46, v50 offset:21120
	ds_write_b32 v46, v49 offset:21184
.Lagg_w0_done:
	s_mov_b64 exec, s[60:61]
	s_waitcnt lgkmcnt(0)
	s_barrier
	ds_read_b32 v46, v45 offset:21120
	v_mov_b32_e32 v47, 0
	ds_read_b32 v48, v47 offset:21212
	ds_read_b32 v49, v47 offset:21244
	ds_read_b32 v50, v55 offset:20544
	v_sub_u32_e32 v41, v41, v40
	v_mul_u32_u24_e32 v47, 0xc4, v53
	s_waitcnt lgkmcnt(0)
	v_add_u32_e32 v41, v41, v46
	ds_write_b32 v62, v41 offset:14336
	v_add_u32_e32 v50, v50, v51
	v_add_lshl_u32 v50, v50, v47, 1
	v_cmp_gt_u32_e32 vcc, 0x188, v52
	s_and_saveexec_b64 s[60:61], vcc
	ds_write_b16 v50, v54 offset:18432
	s_mov_b64 exec, s[60:61]
	v_max_u32_e32 v48, v48, v49
	s_nop 0
	v_readfirstlane_b32 s52, v48
	s_max_u32 s52, s52, s38
	s_max_u32 s52, s52, s39
	s_cmpk_le_u32 s52, 0xe00
	s_cselect_b32 s7, 1, 0
	s_waitcnt lgkmcnt(0)
	s_barrier
	s_cmp_eq_u32 s7, 0
	s_cbranch_scc1 .Lagg_scatter_done
	v_bfe_u32 v48, v8, 16, 7
	v_bfe_u32 v42, v8, 23, 1
	v_and_b32_e32 v44, 0xffff, v8
	v_mad_u32_u24 v48, v42, s55, v48
	v_cmp_le_u32_e32 vcc, s47, v44
	v_lshlrev_b32_e32 v48, 2, v48
	s_nop 0
	v_cndmask_b32_e32 v42, 0, v43, vcc
	v_lshl_add_u32 v48, v42, 2, v48
	ds_read_b32 v48, v48 offset:14336
	v_bfe_u32 v49, v9, 16, 7
	v_bfe_u32 v42, v9, 23, 1
	v_and_b32_e32 v44, 0xffff, v9
	v_mad_u32_u24 v49, v42, s55, v49
	v_cmp_le_u32_e32 vcc, s47, v44
	v_lshlrev_b32_e32 v49, 2, v49
	s_nop 0
	v_cndmask_b32_e32 v42, 0, v43, vcc
	v_lshl_add_u32 v49, v42, 2, v49
	ds_read_b32 v49, v49 offset:14336
	v_bfe_u32 v50, v10, 16, 7
	v_bfe_u32 v42, v10, 23, 1
	v_and_b32_e32 v44, 0xffff, v10
	v_mad_u32_u24 v50, v42, s55, v50
	v_cmp_le_u32_e32 vcc, s47, v44
	v_lshlrev_b32_e32 v50, 2, v50
	s_nop 0
	v_cndmask_b32_e32 v42, 0, v43, vcc
	v_lshl_add_u32 v50, v42, 2, v50
	ds_read_b32 v50, v50 offset:14336
	v_bfe_u32 v51, v11, 16, 7
	v_bfe_u32 v42, v11, 23, 1
	v_and_b32_e32 v44, 0xffff, v11
	v_mad_u32_u24 v51, v42, s55, v51
	v_cmp_le_u32_e32 vcc, s47, v44
	v_lshlrev_b32_e32 v51, 2, v51
	s_nop 0
	v_cndmask_b32_e32 v42, 0, v43, vcc
	v_lshl_add_u32 v51, v42, 2, v51
	ds_read_b32 v51, v51 offset:14336
	s_waitcnt lgkmcnt(3)
	v_add_u32_e32 v48, v48, v16
	v_lshlrev_b32_e32 v48, 1, v48
	s_waitcnt lgkmcnt(2)
	v_add_u32_e32 v49, v49, v17
	v_lshlrev_b32_e32 v49, 1, v49
	s_waitcnt lgkmcnt(1)
	v_add_u32_e32 v50, v50, v18
	v_lshlrev_b32_e32 v50, 1, v50
	s_waitcnt lgkmcnt(0)
	v_add_u32_e32 v51, v51, v19
	v_lshlrev_b32_e32 v51, 1, v51
	v_cmp_gt_u32_e32 vcc, s38, v0
	s_and_saveexec_b64 s[60:61], vcc
	ds_write_b16 v48, v8 offset:0
	s_mov_b64 exec, s[60:61]
	v_add_u32_e32 v40, 0x400, v0
	v_cmp_gt_u32_e32 vcc, s38, v40
	s_and_saveexec_b64 s[60:61], vcc
	ds_write_b16 v49, v9 offset:0
	s_mov_b64 exec, s[60:61]
	v_add_u32_e32 v40, 0x800, v0
	v_cmp_gt_u32_e32 vcc, s38, v40
	s_and_saveexec_b64 s[60:61], vcc
	ds_write_b16 v50, v10 offset:0
	s_mov_b64 exec, s[60:61]
	v_add_u32_e32 v40, 0xc00, v0
	v_cmp_gt_u32_e32 vcc, s38, v40
	s_and_saveexec_b64 s[60:61], vcc
	ds_write_b16 v51, v11 offset:0
	s_mov_b64 exec, s[60:61]
	v_bfe_u32 v48, v24, 16, 7
	v_bfe_u32 v42, v24, 23, 1
	v_and_b32_e32 v44, 0xffff, v24
	v_mad_u32_u24 v48, v42, s55, v48
	v_cmp_le_u32_e32 vcc, s47, v44
	v_lshlrev_b32_e32 v48, 2, v48
	s_nop 0
	v_cndmask_b32_e32 v42, 0, v43, vcc
	v_lshl_add_u32 v48, v42, 2, v48
	ds_read_b32 v48, v48 offset:16384
	v_bfe_u32 v49, v25, 16, 7
	v_bfe_u32 v42, v25, 23, 1
	v_and_b32_e32 v44, 0xffff, v25
	v_mad_u32_u24 v49, v42, s55, v49
	v_cmp_le_u32_e32 vcc, s47, v44
	v_lshlrev_b32_e32 v49, 2, v49
	s_nop 0
	v_cndmask_b32_e32 v42, 0, v43, vcc
	v_lshl_add_u32 v49, v42, 2, v49
	ds_read_b32 v49, v49 offset:16384
	v_bfe_u32 v50, v26, 16, 7
	v_bfe_u32 v42, v26, 23, 1
	v_and_b32_e32 v44, 0xffff, v26
	v_mad_u32_u24 v50, v42, s55, v50
	v_cmp_le_u32_e32 vcc, s47, v44
	v_lshlrev_b32_e32 v50, 2, v50
	s_nop 0
	v_cndmask_b32_e32 v42, 0, v43, vcc
	v_lshl_add_u32 v50, v42, 2, v50
	ds_read_b32 v50, v50 offset:16384
	v_bfe_u32 v51, v27, 16, 7
	v_bfe_u32 v42, v27, 23, 1
	v_and_b32_e32 v44, 0xffff, v27
	v_mad_u32_u24 v51, v42, s55, v51
	v_cmp_le_u32_e32 vcc, s47, v44
	v_lshlrev_b32_e32 v51, 2, v51
	s_nop 0
	v_cndmask_b32_e32 v42, 0, v43, vcc
	v_lshl_add_u32 v51, v42, 2, v51
	ds_read_b32 v51, v51 offset:16384
	s_waitcnt lgkmcnt(3)
	v_add_u32_e32 v48, v48, v20
	v_lshlrev_b32_e32 v48, 1, v48
	s_waitcnt lgkmcnt(2)
	v_add_u32_e32 v49, v49, v21
	v_lshlrev_b32_e32 v49, 1, v49
	s_waitcnt lgkmcnt(1)
	v_add_u32_e32 v50, v50, v22
	v_lshlrev_b32_e32 v50, 1, v50
	s_waitcnt lgkmcnt(0)
	v_add_u32_e32 v51, v51, v23
	v_lshlrev_b32_e32 v51, 1, v51
	v_cmp_gt_u32_e32 vcc, s39, v0
	s_and_saveexec_b64 s[60:61], vcc
	ds_write_b16 v48, v24 offset:7168
	s_mov_b64 exec, s[60:61]
	v_add_u32_e32 v40, 0x400, v0
	v_cmp_gt_u32_e32 vcc, s39, v40
	s_and_saveexec_b64 s[60:61], vcc
	ds_write_b16 v49, v25 offset:7168
	s_mov_b64 exec, s[60:61]
	v_add_u32_e32 v40, 0x800, v0
	v_cmp_gt_u32_e32 vcc, s39, v40
	s_and_saveexec_b64 s[60:61], vcc
	ds_write_b16 v50, v26 offset:7168
	s_mov_b64 exec, s[60:61]
	v_add_u32_e32 v40, 0xc00, v0
	v_cmp_gt_u32_e32 vcc, s39, v40
	s_and_saveexec_b64 s[60:61], vcc
	ds_write_b16 v51, v27 offset:7168
	s_mov_b64 exec, s[60:61]
.Lagg_scatter_done:
	s_waitcnt vmcnt(0) lgkmcnt(0)
	s_barrier
	v_lshrrev_b32_e32 v40, 6, v0
	s_nop 0
	v_readfirstlane_b32 s41, v40
	s_cmp_gt_u32 s41, 12
	s_cbranch_scc1 .Lagg_exit
	v_mov_b32_e32 v15, 1.0
	s_lshl_b32 s52, s3, 8
	s_add_u32 s68, s30, s52
	s_addc_u32 s69, s31, 0
	s_mul_i32 s52, s3, 0x61a800
	s_add_u32 s70, s14, s52
	s_addc_u32 s71, s15, 0
	s_mul_i32 s52, s3, 0x61a800
	s_add_u32 s48, s12, s52
	s_addc_u32 s49, s13, 0
	s_lshl_b32 s52, s3, 7
	s_add_u32 s52, s18, s52
	s_addc_u32 s53, s19, 0
	v_lshlrev_b32_e32 v40, 1, v1
	global_load_dwordx4 v[16:19], v40, s[52:53]
	global_load_dwordx4 v[20:23], v40, s[52:53] offset:16
	global_load_dword v56, v13, s[20:21] offset:0
	global_load_dword v57, v13, s[20:21] offset:16
	s_waitcnt vmcnt(0)
	v_not_b32_e32 v58, v56
	v_and_b32_e32 v59, 0x7fffffff, v56
	v_cmp_gt_i32_e32 vcc, 0, v56
	s_nop 1
	v_cndmask_b32_e32 v56, v58, v59, vcc
	v_not_b32_e32 v58, v57
	v_and_b32_e32 v59, 0x7fffffff, v57
	v_cmp_gt_i32_e32 vcc, 0, v57
	s_nop 1
	v_cndmask_b32_e32 v57, v58, v59, vcc
	v_mov_b32_e32 v46, v56
	v_add_f32_e32 v14, v56, v57
	v_mul_f32_e32 v58, 0x3c23d70a, v14
	v_max_f32_e32 v14, v14, v58
	s_cmp_eq_u32 s7, 0
	s_cbranch_scc1 .Lagg_slow_0
	s_lshl_b32 s40, s41, 4
	v_bfe_u32 v63, v0, 2, 4
	v_add_u32_e32 v63, s40, v63
	v_cmp_gt_u32_e32 vcc, 0xc4, v63
	s_and_saveexec_b64 s[58:59], vcc
	s_cbranch_execz .Lagg_phasedone_0_0
	v_lshlrev_b32_e32 v63, 1, v63
	ds_read_u16 v60, v63 offset:18432
	v_lshrrev_b32_e32 v63, 2, v1
	s_waitcnt lgkmcnt(0)
	v_lshlrev_b32_e32 v61, 2, v60
	ds_read_b32 v58, v61 offset:14336
	ds_read_b32 v59, v61 offset:14340
	v_add_u32_e32 v57, s6, v60
	v_min_u32_e32 v57, 0xc34f, v57
	v_lshlrev_b32_e32 v57, 6, v57
	v_add3_u32 v57, v57, v13, 16
	global_load_dword v57, v57, s[16:17] offset:0
	v_lshl_add_u32 v61, v60, 4, v63
	v_mov_b32_e32 v45, 0
	v_mov_b32_e32 v48, 0
	v_mov_b32_e32 v49, 0
	v_mov_b32_e32 v50, 0
	v_mov_b32_e32 v51, 0
	v_mov_b32_e32 v52, 0
	v_mov_b32_e32 v53, 0
	v_mov_b32_e32 v54, 0
	v_mov_b32_e32 v55, 0
	s_waitcnt lgkmcnt(0)
	v_lshlrev_b32_e32 v41, 1, v58
	v_lshlrev_b32_e32 v42, 1, v59
	v_cmp_lt_u32_e32 vcc, v41, v42
	s_and_saveexec_b64 s[64:65], vcc
	s_cbranch_execz .Lagg_listdone_0_0
	ds_read_u16 v40, v41
	v_add_u32_e32 v41, 2, v41
	s_waitcnt lgkmcnt(0)
	v_mad_u32_u16 v24, v40, s46, v1
	global_load_dwordx4 v[28:31], v24, s[48:49] offset:64
	global_load_dwordx4 v[24:27], v24, s[48:49]
	s_waitcnt vmcnt(2)
	v_add_f32_e32 v47, v46, v57
	v_mul_f32_e32 v56, 0x3c23d70a, v47
	v_max_f32_e32 v47, v47, v56
	v_sub_f32_e32 v43, v57, v47
	v_mul_f32_e32 v43, 0.5, v43
	v_mul_f32_e32 v44, 0xbf7d70a4, v47
.Lagg_loop_0_0:
	v_cmp_lt_u32_e32 vcc, v41, v42
	v_mov_b32_e32 v56, v43
	s_and_b64 s[60:61], exec, vcc
	s_cbranch_scc0 .Lagg_lastA_0_0
	s_mov_b64 s[62:63], exec
	s_mov_b64 exec, s[60:61]
	ds_read_u16 v40, v41
	v_add_u32_e32 v41, 2, v41
	s_waitcnt lgkmcnt(0)
	v_mad_u32_u16 v32, v40, s46, v1
	global_load_dwordx4 v[36:39], v32, s[48:49] offset:64
	global_load_dwordx4 v[32:35], v32, s[48:49]
	s_mov_b64 exec, s[62:63]
	s_waitcnt vmcnt(0)
	v_dot2c_f32_f16_e32 v56, v24, v16
	v_dot2c_f32_f16_e32 v56, v25, v17
	v_dot2c_f32_f16_e32 v56, v26, v18
	v_dot2c_f32_f16_e32 v56, v27, v19
	v_dot2c_f32_f16_e32 v56, v28, v20
	v_dot2c_f32_f16_e32 v56, v29, v21
	v_dot2c_f32_f16_e32 v56, v30, v22
	v_dot2c_f32_f16_e32 v56, v31, v23
	s_nop 2
	v_add_f32_dpp v56, v56, v56 quad_perm:[1,0,3,2] row_mask:0xf bank_mask:0xf bound_ctrl:1
	s_nop 0
	v_fmamk_f32 v58, v56, 0x3c23d70a, v44
	v_max_f32_e32 v56, v56, v58
	v_exp_f32_e32 v56, v56
	s_nop 0
	v_add_f32_e32 v45, v45, v56
	v_cvt_f16_f32_e32 v58, v56
	s_nop 0
	v_pk_fma_f16 v48, v24, v58, v48 op_sel_hi:[1,0,1]
	v_pk_fma_f16 v49, v25, v58, v49 op_sel_hi:[1,0,1]
	v_pk_fma_f16 v50, v26, v58, v50 op_sel_hi:[1,0,1]
	v_pk_fma_f16 v51, v27, v58, v51 op_sel_hi:[1,0,1]
	v_pk_fma_f16 v52, v28, v58, v52 op_sel_hi:[1,0,1]
	v_pk_fma_f16 v53, v29, v58, v53 op_sel_hi:[1,0,1]
	v_pk_fma_f16 v54, v30, v58, v54 op_sel_hi:[1,0,1]
	v_pk_fma_f16 v55, v31, v58, v55 op_sel_hi:[1,0,1]
	s_mov_b64 exec, s[60:61]
	v_cmp_lt_u32_e32 vcc, v41, v42
	v_mov_b32_e32 v56, v43
	s_and_b64 s[60:61], exec, vcc
	s_cbranch_scc0 .Lagg_lastB_0_0
	s_mov_b64 s[62:63], exec
	s_mov_b64 exec, s[60:61]
	ds_read_u16 v40, v41
	v_add_u32_e32 v41, 2, v41
	s_waitcnt lgkmcnt(0)
	v_mad_u32_u16 v24, v40, s46, v1
	global_load_dwordx4 v[28:31], v24, s[48:49] offset:64
	global_load_dwordx4 v[24:27], v24, s[48:49]
	s_mov_b64 exec, s[62:63]
	s_waitcnt vmcnt(0)
	v_dot2c_f32_f16_e32 v56, v32, v16
	v_dot2c_f32_f16_e32 v56, v33, v17
	v_dot2c_f32_f16_e32 v56, v34, v18
	v_dot2c_f32_f16_e32 v56, v35, v19
	v_dot2c_f32_f16_e32 v56, v36, v20
	v_dot2c_f32_f16_e32 v56, v37, v21
	v_dot2c_f32_f16_e32 v56, v38, v22
	v_dot2c_f32_f16_e32 v56, v39, v23
	s_nop 2
	v_add_f32_dpp v56, v56, v56 quad_perm:[1,0,3,2] row_mask:0xf bank_mask:0xf bound_ctrl:1
	s_nop 0
	v_fmamk_f32 v58, v56, 0x3c23d70a, v44
	v_max_f32_e32 v56, v56, v58
	v_exp_f32_e32 v56, v56
	s_nop 0
	v_add_f32_e32 v45, v45, v56
	v_cvt_f16_f32_e32 v58, v56
	s_nop 0
	v_pk_fma_f16 v48, v32, v58, v48 op_sel_hi:[1,0,1]
	v_pk_fma_f16 v49, v33, v58, v49 op_sel_hi:[1,0,1]
	v_pk_fma_f16 v50, v34, v58, v50 op_sel_hi:[1,0,1]
	v_pk_fma_f16 v51, v35, v58, v51 op_sel_hi:[1,0,1]
	v_pk_fma_f16 v52, v36, v58, v52 op_sel_hi:[1,0,1]
	v_pk_fma_f16 v53, v37, v58, v53 op_sel_hi:[1,0,1]
	v_pk_fma_f16 v54, v38, v58, v54 op_sel_hi:[1,0,1]
	v_pk_fma_f16 v55, v39, v58, v55 op_sel_hi:[1,0,1]
	s_mov_b64 exec, s[60:61]
	s_branch .Lagg_loop_0_0

.Lagg_listdone_0_0:
	s_mov_b64 exec, s[64:65]
	s_waitcnt vmcnt(0)
	ds_write_b32 v61, v48 offset:21248
	ds_write_b32 v61, v49 offset:24384
	ds_write_b32 v61, v50 offset:27520
	ds_write_b32 v61, v51 offset:30656
	ds_write_b32 v61, v52 offset:33792
	ds_write_b32 v61, v53 offset:36928
	ds_write_b32 v61, v54 offset:40064
	ds_write_b32 v61, v55 offset:43200
	ds_write_b32 v61, v45 offset:46336
.Lagg_phasedone_0_0:
	s_mov_b64 exec, s[58:59]
	s_sub_u32 s40, 12, s41
	s_lshl_b32 s40, s40, 4
	v_bfe_u32 v63, v0, 2, 4
	v_add_u32_e32 v63, s40, v63
	v_cmp_gt_u32_e32 vcc, 0xc4, v63
	s_and_saveexec_b64 s[58:59], vcc
	s_cbranch_execz .Lagg_phasedone_0_1
	v_lshlrev_b32_e32 v63, 1, v63
	ds_read_u16 v60, v63 offset:18824
	v_lshrrev_b32_e32 v63, 2, v1
	s_waitcnt lgkmcnt(0)
	v_lshlrev_b32_e32 v61, 2, v60
	ds_read_b32 v58, v61 offset:15120
	ds_read_b32 v59, v61 offset:15124
	v_add_u32_e32 v57, s6, v60
	v_min_u32_e32 v57, 0xc34f, v57
	v_lshlrev_b32_e32 v57, 6, v57
	v_add3_u32 v57, v57, v13, 16
	global_load_dword v57, v57, s[16:17] offset:0
	v_lshl_add_u32 v61, v60, 4, v63
	v_add_u32_e32 v61, 0x6e40, v61
	v_mov_b32_e32 v45, 0
	v_mov_b32_e32 v48, 0
	v_mov_b32_e32 v49, 0
	v_mov_b32_e32 v50, 0
	v_mov_b32_e32 v51, 0
	v_mov_b32_e32 v52, 0
	v_mov_b32_e32 v53, 0
	v_mov_b32_e32 v54, 0
	v_mov_b32_e32 v55, 0
	s_waitcnt lgkmcnt(0)
	v_lshlrev_b32_e32 v41, 1, v58
	v_lshlrev_b32_e32 v42, 1, v59
	v_cmp_lt_u32_e32 vcc, v41, v42
	s_and_saveexec_b64 s[64:65], vcc
	s_cbranch_execz .Lagg_listdone_0_1
	ds_read_u16 v40, v41
	v_add_u32_e32 v41, 2, v41
	s_waitcnt lgkmcnt(0)
	v_mad_u32_u16 v24, v40, s46, v1
	global_load_dwordx4 v[28:31], v24, s[48:49] offset:64
	global_load_dwordx4 v[24:27], v24, s[48:49]
	s_waitcnt vmcnt(2)
	v_add_f32_e32 v47, v46, v57
	v_mul_f32_e32 v56, 0x3c23d70a, v47
	v_max_f32_e32 v47, v47, v56
	v_sub_f32_e32 v43, v57, v47
	v_mul_f32_e32 v43, 0.5, v43
	v_mul_f32_e32 v44, 0xbf7d70a4, v47

.Lagg_join_0:
	s_waitcnt vmcnt(0) lgkmcnt(0)
	s_barrier
	v_cmp_gt_u32_e32 vcc, s5, v2
	s_and_saveexec_b64 s[58:59], vcc
	v_lshlrev_b32_e32 v61, 2, v0
	v_add_u32_e32 v60, 0x6e40, v61
	ds_read_b32 v48, v61 offset:21248
	ds_read_b32 v49, v61 offset:24384
	ds_read_b32 v50, v61 offset:27520
	ds_read_b32 v51, v61 offset:30656
	ds_read_b32 v52, v61 offset:33792
	ds_read_b32 v53, v61 offset:36928
	ds_read_b32 v54, v61 offset:40064
	ds_read_b32 v55, v61 offset:43200
	ds_read_b32 v45, v61 offset:46336
	s_waitcnt lgkmcnt(0)
	ds_read_b32 v24, v60 offset:21248
	ds_read_b32 v25, v60 offset:24384
	ds_read_b32 v26, v60 offset:27520
	ds_read_b32 v27, v60 offset:30656
	ds_read_b32 v28, v60 offset:33792
	ds_read_b32 v29, v60 offset:36928
	ds_read_b32 v30, v60 offset:40064
	ds_read_b32 v31, v60 offset:43200
	ds_read_b32 v32, v60 offset:46336
	v_mov_b32_e32 v62, 0x3c003c00
	s_waitcnt lgkmcnt(0)
	s_barrier
	v_pk_fma_f16 v48, v24, v62, v48
	v_pk_fma_f16 v49, v25, v62, v49
	v_pk_fma_f16 v50, v26, v62, v50
	v_pk_fma_f16 v51, v27, v62, v51
	v_pk_fma_f16 v52, v28, v62, v52
	v_pk_fma_f16 v53, v29, v62, v53
	v_pk_fma_f16 v54, v30, v62, v54
	v_pk_fma_f16 v55, v31, v62, v55
	v_add_f32_e32 v45, v45, v32
	s_cbranch_execz .Lagg_end_0
	v_add_f32_e32 v47, v46, v3
	v_mul_f32_e32 v58, 0x3c23d70a, v47
	v_max_f32_e32 v47, v47, v58
	v_sub_f32_e32 v58, v14, v47
	v_exp_f32_e32 v58, v58
	v_mul_f32_e32 v59, 0x33000000, v45
	v_rcp_f32_e32 v42, v45
	v_mul_f32_e32 v58, 0x24e69595, v58
	v_fma_f32 v60, -v45, v42, 1.0
	v_cmp_ge_f32_e64 s[62:63], v59, v58
	v_cmp_eq_f32_e32 vcc, 0, v45
	v_fmac_f32_e32 v42, v60, v42
	s_nop 1
	v_cndmask_b32_e64 v42, v42, 0, vcc
	s_or_b64 s[62:63], s[62:63], vcc
	s_mov_b64 s[66:67], exec
	s_andn2_b64 exec, exec, s[62:63]
	s_cbranch_execnz .Lagg_gmax_0
.Lagg_gmaxret_0:
	s_mov_b64 exec, s[66:67]
	v_fma_mix_f32 v32, v48, v42, 0 op_sel_hi:[1,0,0]
	v_fma_mix_f32 v33, v48, v42, 0 op_sel:[1,0,0] op_sel_hi:[1,0,0]
	v_fma_mix_f32 v34, v49, v42, 0 op_sel_hi:[1,0,0]
	v_fma_mix_f32 v35, v49, v42, 0 op_sel:[1,0,0] op_sel_hi:[1,0,0]
	v_fma_mix_f32 v36, v50, v42, 0 op_sel_hi:[1,0,0]
	v_fma_mix_f32 v37, v50, v42, 0 op_sel:[1,0,0] op_sel_hi:[1,0,0]
	v_fma_mix_f32 v38, v51, v42, 0 op_sel_hi:[1,0,0]
	v_fma_mix_f32 v39, v51, v42, 0 op_sel:[1,0,0] op_sel_hi:[1,0,0]
	v_fma_mix_f32 v56, v52, v42, 0 op_sel_hi:[1,0,0]
	v_fma_mix_f32 v57, v52, v42, 0 op_sel:[1,0,0] op_sel_hi:[1,0,0]
	v_fma_mix_f32 v58, v53, v42, 0 op_sel_hi:[1,0,0]
	v_fma_mix_f32 v59, v53, v42, 0 op_sel:[1,0,0] op_sel_hi:[1,0,0]
	v_fma_mix_f32 v60, v54, v42, 0 op_sel_hi:[1,0,0]
	v_fma_mix_f32 v61, v54, v42, 0 op_sel:[1,0,0] op_sel_hi:[1,0,0]
	v_fma_mix_f32 v62, v55, v42, 0 op_sel_hi:[1,0,0]
	v_fma_mix_f32 v63, v55, v42, 0 op_sel:[1,0,0] op_sel_hi:[1,0,0]
	v_cvt_pk_f16_f32 v5, v32, v33
	v_cvt_pk_f16_f32 v6, v34, v35
	v_cvt_pk_f16_f32 v7, v36, v37
	v_cvt_pk_f16_f32 v8, v38, v39
	v_cvt_pk_f16_f32 v9, v56, v57
	v_cvt_pk_f16_f32 v10, v58, v59
	v_cvt_pk_f16_f32 v11, v60, v61
	v_cvt_pk_f16_f32 v12, v62, v63
.Lagg_end_0:
	s_mov_b64 exec, s[58:59]
	s_mul_i32 s52, s3, 0x61a800
	s_add_u32 s52, s52, 0xc35000
	s_add_u32 s48, s12, s52
	s_addc_u32 s49, s13, 0
	s_lshl_b32 s52, s3, 7
	s_add_u32 s52, s52, 0x100
	s_add_u32 s52, s18, s52
	s_addc_u32 s53, s19, 0
	v_lshlrev_b32_e32 v40, 1, v1
	global_load_dwordx4 v[16:19], v40, s[52:53]
	global_load_dwordx4 v[20:23], v40, s[52:53] offset:16
	global_load_dword v56, v13, s[20:21] offset:32
	global_load_dword v57, v13, s[20:21] offset:48
	s_waitcnt vmcnt(0)
	v_not_b32_e32 v58, v56
	v_and_b32_e32 v59, 0x7fffffff, v56
	v_cmp_gt_i32_e32 vcc, 0, v56
	s_nop 1
	v_cndmask_b32_e32 v56, v58, v59, vcc
	v_not_b32_e32 v58, v57
	v_and_b32_e32 v59, 0x7fffffff, v57
	v_cmp_gt_i32_e32 vcc, 0, v57
	s_nop 1
	v_cndmask_b32_e32 v57, v58, v59, vcc
	v_mov_b32_e32 v46, v56
	v_add_f32_e32 v14, v56, v57
	v_mul_f32_e32 v58, 0x3c23d70a, v14
	v_max_f32_e32 v14, v14, v58
	s_cmp_eq_u32 s7, 0
	s_cbranch_scc1 .Lagg_slow_1
	s_sub_u32 s40, 12, s41
	s_lshl_b32 s40, s40, 4
	v_bfe_u32 v63, v0, 2, 4
	v_add_u32_e32 v63, s40, v63
	v_cmp_gt_u32_e32 vcc, 0xc4, v63
	s_and_saveexec_b64 s[58:59], vcc
	s_cbranch_execz .Lagg_phasedone_1_0
	v_lshlrev_b32_e32 v63, 1, v63
	ds_read_u16 v60, v63 offset:19216
	v_lshrrev_b32_e32 v63, 2, v1
	s_waitcnt lgkmcnt(0)
	v_lshlrev_b32_e32 v61, 2, v60
	ds_read_b32 v58, v61 offset:16384
	ds_read_b32 v59, v61 offset:16388
	v_add_u32_e32 v57, s6, v60
	v_min_u32_e32 v57, 0xc34f, v57
	v_lshlrev_b32_e32 v57, 6, v57
	v_add3_u32 v57, v57, v13, 16
	global_load_dword v57, v57, s[16:17] offset:32
	v_lshl_add_u32 v61, v60, 4, v63
	v_mov_b32_e32 v45, 0
	v_mov_b32_e32 v48, 0
	v_mov_b32_e32 v49, 0
	v_mov_b32_e32 v50, 0
	v_mov_b32_e32 v51, 0
	v_mov_b32_e32 v52, 0
	v_mov_b32_e32 v53, 0
	v_mov_b32_e32 v54, 0
	v_mov_b32_e32 v55, 0
	s_waitcnt lgkmcnt(0)
	v_lshlrev_b32_e32 v41, 1, v58
	v_lshlrev_b32_e32 v42, 1, v59
	v_add_u32_e32 v41, 0x1c00, v41
	v_add_u32_e32 v42, 0x1c00, v42
	v_cmp_lt_u32_e32 vcc, v41, v42
	s_and_saveexec_b64 s[64:65], vcc
	s_cbranch_execz .Lagg_listdone_1_0
	ds_read_u16 v40, v41
	v_add_u32_e32 v41, 2, v41
	s_waitcnt lgkmcnt(0)
	v_mad_u32_u16 v24, v40, s46, v1
	global_load_dwordx4 v[28:31], v24, s[48:49] offset:64
	global_load_dwordx4 v[24:27], v24, s[48:49]
	s_waitcnt vmcnt(2)
	v_add_f32_e32 v47, v46, v57
	v_mul_f32_e32 v56, 0x3c23d70a, v47
	v_max_f32_e32 v47, v47, v56
	v_sub_f32_e32 v43, v57, v47
	v_mul_f32_e32 v43, 0.5, v43
	v_mul_f32_e32 v44, 0xbf7d70a4, v47

.Lagg_phasedone_1_0:
	s_mov_b64 exec, s[58:59]
	s_lshl_b32 s40, s41, 4
	v_bfe_u32 v63, v0, 2, 4
	v_add_u32_e32 v63, s40, v63
	v_cmp_gt_u32_e32 vcc, 0xc4, v63
	s_and_saveexec_b64 s[58:59], vcc
	s_cbranch_execz .Lagg_phasedone_1_1
	v_lshlrev_b32_e32 v63, 1, v63
	ds_read_u16 v60, v63 offset:19608
	v_lshrrev_b32_e32 v63, 2, v1
	s_waitcnt lgkmcnt(0)
	v_lshlrev_b32_e32 v61, 2, v60
	ds_read_b32 v58, v61 offset:17168
	ds_read_b32 v59, v61 offset:17172
	v_add_u32_e32 v57, s6, v60
	v_min_u32_e32 v57, 0xc34f, v57
	v_lshlrev_b32_e32 v57, 6, v57
	v_add3_u32 v57, v57, v13, 16
	global_load_dword v57, v57, s[16:17] offset:32
	v_lshl_add_u32 v61, v60, 4, v63
	v_add_u32_e32 v61, 0x6e40, v61
	v_mov_b32_e32 v45, 0
	v_mov_b32_e32 v48, 0
	v_mov_b32_e32 v49, 0
	v_mov_b32_e32 v50, 0
	v_mov_b32_e32 v51, 0
	v_mov_b32_e32 v52, 0
	v_mov_b32_e32 v53, 0
	v_mov_b32_e32 v54, 0
	v_mov_b32_e32 v55, 0
	s_waitcnt lgkmcnt(0)
	v_lshlrev_b32_e32 v41, 1, v58
	v_lshlrev_b32_e32 v42, 1, v59
	v_add_u32_e32 v41, 0x1c00, v41
	v_add_u32_e32 v42, 0x1c00, v42
	v_cmp_lt_u32_e32 vcc, v41, v42
	s_and_saveexec_b64 s[64:65], vcc
	s_cbranch_execz .Lagg_listdone_1_1
	ds_read_u16 v40, v41
	v_add_u32_e32 v41, 2, v41
	s_waitcnt lgkmcnt(0)
	v_mad_u32_u16 v24, v40, s46, v1
	global_load_dwordx4 v[28:31], v24, s[48:49] offset:64
	global_load_dwordx4 v[24:27], v24, s[48:49]
	s_waitcnt vmcnt(2)
	v_add_f32_e32 v47, v46, v57
	v_mul_f32_e32 v56, 0x3c23d70a, v47
	v_max_f32_e32 v47, v47, v56
	v_sub_f32_e32 v43, v57, v47
	v_mul_f32_e32 v43, 0.5, v43
	v_mul_f32_e32 v44, 0xbf7d70a4, v47

.Lagg_join_1:
	s_waitcnt vmcnt(0) lgkmcnt(0)
	s_barrier
	v_cmp_gt_u32_e32 vcc, s5, v2
	s_and_saveexec_b64 s[58:59], vcc
	v_lshlrev_b32_e32 v61, 2, v0
	v_add_u32_e32 v60, 0x6e40, v61
	ds_read_b32 v48, v61 offset:21248
	ds_read_b32 v49, v61 offset:24384
	ds_read_b32 v50, v61 offset:27520
	ds_read_b32 v51, v61 offset:30656
	ds_read_b32 v52, v61 offset:33792
	ds_read_b32 v53, v61 offset:36928
	ds_read_b32 v54, v61 offset:40064
	ds_read_b32 v55, v61 offset:43200
	ds_read_b32 v45, v61 offset:46336
	s_waitcnt lgkmcnt(0)
	ds_read_b32 v24, v60 offset:21248
	ds_read_b32 v25, v60 offset:24384
	ds_read_b32 v26, v60 offset:27520
	ds_read_b32 v27, v60 offset:30656
	ds_read_b32 v28, v60 offset:33792
	ds_read_b32 v29, v60 offset:36928
	ds_read_b32 v30, v60 offset:40064
	ds_read_b32 v31, v60 offset:43200
	ds_read_b32 v32, v60 offset:46336
	v_mov_b32_e32 v62, 0x3c003c00
	s_waitcnt lgkmcnt(0)
	s_barrier
	v_pk_fma_f16 v48, v24, v62, v48
	v_pk_fma_f16 v49, v25, v62, v49
	v_pk_fma_f16 v50, v26, v62, v50
	v_pk_fma_f16 v51, v27, v62, v51
	v_pk_fma_f16 v52, v28, v62, v52
	v_pk_fma_f16 v53, v29, v62, v53
	v_pk_fma_f16 v54, v30, v62, v54
	v_pk_fma_f16 v55, v31, v62, v55
	v_add_f32_e32 v45, v45, v32
	s_cbranch_execz .Lagg_end_1
	v_add_f32_e32 v47, v46, v4
	v_mul_f32_e32 v58, 0x3c23d70a, v47
	v_max_f32_e32 v47, v47, v58
	v_add_u32_e32 v61, s6, v2
	v_mad_u32_u24 v40, v61, s46, v1
	global_load_dwordx4 v[24:27], v40, s[70:71] nt
	global_load_dwordx4 v[28:31], v40, s[70:71] offset:64 nt
	v_lshlrev_b32_e32 v41, 9, v61
	v_lshl_add_u32 v41, v1, 2, v41
	v_sub_f32_e32 v58, v14, v47
	v_exp_f32_e32 v58, v58
	v_mul_f32_e32 v59, 0x33000000, v45
	v_rcp_f32_e32 v42, v45
	v_mul_f32_e32 v58, 0x24e69595, v58
	v_fma_f32 v60, -v45, v42, 1.0
	v_cmp_ge_f32_e64 s[62:63], v59, v58
	v_cmp_eq_f32_e32 vcc, 0, v45
	v_fmac_f32_e32 v42, v60, v42
	s_nop 1
	v_cndmask_b32_e64 v42, v42, 0, vcc
	s_or_b64 s[62:63], s[62:63], vcc
	s_mov_b64 s[66:67], exec
	s_andn2_b64 exec, exec, s[62:63]
	s_cbranch_execnz .Lagg_gmax_1
.Lagg_gmaxret_1:
	s_mov_b64 exec, s[66:67]
	v_fma_mix_f32 v32, v48, v42, 0 op_sel_hi:[1,0,0]
	v_fma_mix_f32 v33, v48, v42, 0 op_sel:[1,0,0] op_sel_hi:[1,0,0]
	v_fma_mix_f32 v34, v49, v42, 0 op_sel_hi:[1,0,0]
	v_fma_mix_f32 v35, v49, v42, 0 op_sel:[1,0,0] op_sel_hi:[1,0,0]
	v_fma_mix_f32 v36, v50, v42, 0 op_sel_hi:[1,0,0]
	v_fma_mix_f32 v37, v50, v42, 0 op_sel:[1,0,0] op_sel_hi:[1,0,0]
	v_fma_mix_f32 v38, v51, v42, 0 op_sel_hi:[1,0,0]
	v_fma_mix_f32 v39, v51, v42, 0 op_sel:[1,0,0] op_sel_hi:[1,0,0]
	v_fma_mix_f32 v56, v52, v42, 0 op_sel_hi:[1,0,0]
	v_fma_mix_f32 v57, v52, v42, 0 op_sel:[1,0,0] op_sel_hi:[1,0,0]
	v_fma_mix_f32 v58, v53, v42, 0 op_sel_hi:[1,0,0]
	v_fma_mix_f32 v59, v53, v42, 0 op_sel:[1,0,0] op_sel_hi:[1,0,0]
	v_fma_mix_f32 v60, v54, v42, 0 op_sel_hi:[1,0,0]
	v_fma_mix_f32 v61, v54, v42, 0 op_sel:[1,0,0] op_sel_hi:[1,0,0]
	v_fma_mix_f32 v62, v55, v42, 0 op_sel_hi:[1,0,0]
	v_fma_mix_f32 v63, v55, v42, 0 op_sel:[1,0,0] op_sel_hi:[1,0,0]
	v_fma_mix_f32 v32, v5, v15, v32 op_sel_hi:[1,0,0]
	v_fma_mix_f32 v33, v5, v15, v33 op_sel:[1,0,0] op_sel_hi:[1,0,0]
	v_fma_mix_f32 v34, v6, v15, v34 op_sel_hi:[1,0,0]
	v_fma_mix_f32 v35, v6, v15, v35 op_sel:[1,0,0] op_sel_hi:[1,0,0]
	v_fma_mix_f32 v36, v7, v15, v36 op_sel_hi:[1,0,0]
	v_fma_mix_f32 v37, v7, v15, v37 op_sel:[1,0,0] op_sel_hi:[1,0,0]
	v_fma_mix_f32 v38, v8, v15, v38 op_sel_hi:[1,0,0]
	v_fma_mix_f32 v39, v8, v15, v39 op_sel:[1,0,0] op_sel_hi:[1,0,0]
	v_fma_mix_f32 v56, v9, v15, v56 op_sel_hi:[1,0,0]
	v_fma_mix_f32 v57, v9, v15, v57 op_sel:[1,0,0] op_sel_hi:[1,0,0]
	v_fma_mix_f32 v58, v10, v15, v58 op_sel_hi:[1,0,0]
	v_fma_mix_f32 v59, v10, v15, v59 op_sel:[1,0,0] op_sel_hi:[1,0,0]
	v_fma_mix_f32 v60, v11, v15, v60 op_sel_hi:[1,0,0]
	v_fma_mix_f32 v61, v11, v15, v61 op_sel:[1,0,0] op_sel_hi:[1,0,0]
	v_fma_mix_f32 v62, v12, v15, v62 op_sel_hi:[1,0,0]
	v_fma_mix_f32 v63, v12, v15, v63 op_sel:[1,0,0] op_sel_hi:[1,0,0]
	s_waitcnt vmcnt(0)
	v_fma_mix_f32 v32, v24, v15, v32 op_sel_hi:[1,0,0]
	v_fma_mix_f32 v33, v24, v15, v33 op_sel:[1,0,0] op_sel_hi:[1,0,0]
	v_fma_mix_f32 v34, v25, v15, v34 op_sel_hi:[1,0,0]
	v_fma_mix_f32 v35, v25, v15, v35 op_sel:[1,0,0] op_sel_hi:[1,0,0]
	v_fma_mix_f32 v36, v26, v15, v36 op_sel_hi:[1,0,0]
	v_fma_mix_f32 v37, v26, v15, v37 op_sel:[1,0,0] op_sel_hi:[1,0,0]
	v_fma_mix_f32 v38, v27, v15, v38 op_sel_hi:[1,0,0]
	v_fma_mix_f32 v39, v27, v15, v39 op_sel:[1,0,0] op_sel_hi:[1,0,0]
	v_fma_mix_f32 v56, v28, v15, v56 op_sel_hi:[1,0,0]
	v_fma_mix_f32 v57, v28, v15, v57 op_sel:[1,0,0] op_sel_hi:[1,0,0]
	v_fma_mix_f32 v58, v29, v15, v58 op_sel_hi:[1,0,0]
	v_fma_mix_f32 v59, v29, v15, v59 op_sel:[1,0,0] op_sel_hi:[1,0,0]
	v_fma_mix_f32 v60, v30, v15, v60 op_sel_hi:[1,0,0]
	v_fma_mix_f32 v61, v30, v15, v61 op_sel:[1,0,0] op_sel_hi:[1,0,0]
	v_fma_mix_f32 v62, v31, v15, v62 op_sel_hi:[1,0,0]
	v_fma_mix_f32 v63, v31, v15, v63 op_sel:[1,0,0] op_sel_hi:[1,0,0]
	v_max_f32_e32 v32, 0, v32
	v_max_f32_e32 v33, 0, v33
	v_max_f32_e32 v34, 0, v34
	v_max_f32_e32 v35, 0, v35
	v_max_f32_e32 v36, 0, v36
	v_max_f32_e32 v37, 0, v37
	v_max_f32_e32 v38, 0, v38
	v_max_f32_e32 v39, 0, v39
	v_max_f32_e32 v56, 0, v56
	v_max_f32_e32 v57, 0, v57
	v_max_f32_e32 v58, 0, v58
	v_max_f32_e32 v59, 0, v59
	v_max_f32_e32 v60, 0, v60
	v_max_f32_e32 v61, 0, v61
	v_max_f32_e32 v62, 0, v62
	v_max_f32_e32 v63, 0, v63
	global_store_dwordx4 v41, v[32:35], s[68:69] nt
	global_store_dwordx4 v41, v[36:39], s[68:69] offset:16 nt
	global_store_dwordx4 v41, v[56:59], s[68:69] offset:32 nt
	global_store_dwordx4 v41, v[60:63], s[68:69] offset:48 nt
	s_nop 1
.Lagg_end_1:
	s_mov_b64 exec, s[58:59]
.Lagg_exit:
	s_endpgm
.Lagg_gmax_0:
	v_add_u32_e32 v32, 0, v13
	v_lshrrev_b32_e32 v33, 2, v1
	v_and_b32_e32 v33, 4, v33
	v_mov_b32_e32 v36, 0xff800000
	s_mov_b32 s52, 0
.Lagg_gmaxloop_0:
	global_load_dword v34, v33, s[24:25]
	global_load_dword v35, v33, s[22:23]
	s_waitcnt vmcnt(0)
	v_lshl_add_u32 v34, v34, 6, v32
	v_lshl_add_u32 v35, v35, 6, v32
	global_load_dword v34, v34, s[16:17]
	global_load_dword v35, v35, s[16:17] offset:16
	v_add_u32_e32 v33, 8, v33
	s_add_u32 s52, s52, 2
	s_cmp_lt_u32 s52, 0xc3500
	s_waitcnt vmcnt(0)
	v_add_f32_e32 v34, v34, v35
	v_max_f32_e32 v36, v36, v34
	s_cbranch_scc1 .Lagg_gmaxloop_0
	s_nop 1
	v_mov_b32_dpp v34, v36 quad_perm:[1,0,3,2] row_mask:0xf bank_mask:0xf bound_ctrl:1
	s_nop 0
	v_max_f32_e32 v36, v36, v34
	v_mul_f32_e32 v34, 0x3c23d70a, v36
	v_max_f32_e32 v36, v36, v34
	v_sub_f32_e32 v36, v36, v47
	v_exp_f32_e32 v36, v36
	v_mov_b32_e32 v34, v45
	v_fmac_f32_e32 v34, 0x24e69595, v36
	s_nop 0
	v_rcp_f32_e32 v42, v34
	s_nop 0
	v_fma_f32 v36, -v34, v42, 1.0
	v_fmac_f32_e32 v42, v36, v42
	s_branch .Lagg_gmaxret_0
.Lagg_slow_0:
	v_cmp_gt_u32_e32 vcc, 0xc4, v2
	s_and_saveexec_b64 s[58:59], vcc
	v_add_f32_e32 v47, v46, v3
	v_mul_f32_e32 v56, 0x3c23d70a, v47
	v_max_f32_e32 v47, v47, v56
	v_sub_f32_e32 v43, v3, v47
	v_mul_f32_e32 v43, 0.5, v43
	v_mul_f32_e32 v44, 0xbf7d70a4, v47
	v_mov_b32_e32 v45, 0
	v_mov_b32_e32 v48, 0
	v_mov_b32_e32 v49, 0
	v_mov_b32_e32 v50, 0
	v_mov_b32_e32 v51, 0
	v_mov_b32_e32 v52, 0
	v_mov_b32_e32 v53, 0
	v_mov_b32_e32 v54, 0
	v_mov_b32_e32 v55, 0
	s_mov_b32 s52, 0
	s_mov_b32 s53, 0
	s_cmp_lt_u32 s52, s38
	s_cbranch_scc0 .Lagg_slowdone_0
.Lagg_slowloop_0:
	s_load_dword s54, s[42:43], s53
	s_waitcnt lgkmcnt(0)
	s_bfe_u32 s64, s54, 0x70010
	s_bfe_u32 s65, s54, 0x10017
	s_mul_i32 s65, s65, 0x62
	s_add_u32 s64, s64, s65
	s_and_b32 s54, s54, 0xffff
	s_mul_i32 s54, s54, s46
	v_cmp_eq_u32_e32 vcc, s64, v2
	s_and_saveexec_b64 s[62:63], vcc
	s_cbranch_execz .Lagg_slownext_0
	v_add_u32_e32 v24, s54, v1
	global_load_dwordx4 v[28:31], v24, s[48:49] offset:64
	global_load_dwordx4 v[24:27], v24, s[48:49]
	v_mov_b32_e32 v56, v43
	s_waitcnt vmcnt(0)
	v_dot2c_f32_f16_e32 v56, v24, v16
	v_dot2c_f32_f16_e32 v56, v25, v17
	v_dot2c_f32_f16_e32 v56, v26, v18
	v_dot2c_f32_f16_e32 v56, v27, v19
	v_dot2c_f32_f16_e32 v56, v28, v20
	v_dot2c_f32_f16_e32 v56, v29, v21
	v_dot2c_f32_f16_e32 v56, v30, v22
	v_dot2c_f32_f16_e32 v56, v31, v23
	s_nop 2
	v_add_f32_dpp v56, v56, v56 quad_perm:[1,0,3,2] row_mask:0xf bank_mask:0xf bound_ctrl:1
	s_nop 0
	v_fmamk_f32 v58, v56, 0x3c23d70a, v44
	v_max_f32_e32 v56, v56, v58
	v_exp_f32_e32 v56, v56
	s_nop 0
	v_add_f32_e32 v45, v45, v56
	v_cvt_f16_f32_e32 v58, v56
	s_nop 0
	v_pk_fma_f16 v48, v24, v58, v48 op_sel_hi:[1,0,1]
	v_pk_fma_f16 v49, v25, v58, v49 op_sel_hi:[1,0,1]
	v_pk_fma_f16 v50, v26, v58, v50 op_sel_hi:[1,0,1]
	v_pk_fma_f16 v51, v27, v58, v51 op_sel_hi:[1,0,1]
	v_pk_fma_f16 v52, v28, v58, v52 op_sel_hi:[1,0,1]
	v_pk_fma_f16 v53, v29, v58, v53 op_sel_hi:[1,0,1]
	v_pk_fma_f16 v54, v30, v58, v54 op_sel_hi:[1,0,1]
	v_pk_fma_f16 v55, v31, v58, v55 op_sel_hi:[1,0,1]

.Lagg_slowdone_0:
	v_lshlrev_b32_e32 v61, 2, v0
	ds_write_b32 v61, v48 offset:21248
	ds_write_b32 v61, v49 offset:24384
	ds_write_b32 v61, v50 offset:27520
	ds_write_b32 v61, v51 offset:30656
	ds_write_b32 v61, v52 offset:33792
	ds_write_b32 v61, v53 offset:36928
	ds_write_b32 v61, v54 offset:40064
	ds_write_b32 v61, v55 offset:43200
	ds_write_b32 v61, v45 offset:46336
	v_mov_b32_e32 v40, 0
	v_add_u32_e32 v61, 0x6e40, v61
	ds_write_b32 v61, v40 offset:21248
	ds_write_b32 v61, v40 offset:24384
	ds_write_b32 v61, v40 offset:27520
	ds_write_b32 v61, v40 offset:30656
	ds_write_b32 v61, v40 offset:33792
	ds_write_b32 v61, v40 offset:36928
	ds_write_b32 v61, v40 offset:40064
	ds_write_b32 v61, v40 offset:43200
	ds_write_b32 v61, v40 offset:46336
	s_mov_b64 exec, s[58:59]
	s_branch .Lagg_join_0
.Lagg_gmax_1:
	v_add_u32_e32 v32, 32, v13
	v_lshrrev_b32_e32 v33, 2, v1
	v_and_b32_e32 v33, 4, v33
	v_mov_b32_e32 v36, 0xff800000
	s_mov_b32 s52, 0
.Lagg_gmaxloop_1:
	global_load_dword v34, v33, s[28:29]
	global_load_dword v35, v33, s[26:27]
	s_waitcnt vmcnt(0)
	v_lshl_add_u32 v34, v34, 6, v32
	v_lshl_add_u32 v35, v35, 6, v32
	global_load_dword v34, v34, s[16:17]
	global_load_dword v35, v35, s[16:17] offset:16
	v_add_u32_e32 v33, 8, v33
	s_add_u32 s52, s52, 2
	s_cmp_lt_u32 s52, 0xc3500
	s_waitcnt vmcnt(0)
	v_add_f32_e32 v34, v34, v35
	v_max_f32_e32 v36, v36, v34
	s_cbranch_scc1 .Lagg_gmaxloop_1
	s_nop 1
	v_mov_b32_dpp v34, v36 quad_perm:[1,0,3,2] row_mask:0xf bank_mask:0xf bound_ctrl:1
	s_nop 0
	v_max_f32_e32 v36, v36, v34
	v_mul_f32_e32 v34, 0x3c23d70a, v36
	v_max_f32_e32 v36, v36, v34
	v_sub_f32_e32 v36, v36, v47
	v_exp_f32_e32 v36, v36
	v_mov_b32_e32 v34, v45
	v_fmac_f32_e32 v34, 0x24e69595, v36
	s_nop 0
	v_rcp_f32_e32 v42, v34
	s_nop 0
	v_fma_f32 v36, -v34, v42, 1.0
	v_fmac_f32_e32 v42, v36, v42
	s_branch .Lagg_gmaxret_1
.Lagg_slow_1:
	v_cmp_gt_u32_e32 vcc, 0xc4, v2
	s_and_saveexec_b64 s[58:59], vcc
	v_add_f32_e32 v47, v46, v4
	v_mul_f32_e32 v56, 0x3c23d70a, v47
	v_max_f32_e32 v47, v47, v56
	v_sub_f32_e32 v43, v4, v47
	v_mul_f32_e32 v43, 0.5, v43
	v_mul_f32_e32 v44, 0xbf7d70a4, v47
	v_mov_b32_e32 v45, 0
	v_mov_b32_e32 v48, 0
	v_mov_b32_e32 v49, 0
	v_mov_b32_e32 v50, 0
	v_mov_b32_e32 v51, 0
	v_mov_b32_e32 v52, 0
	v_mov_b32_e32 v53, 0
	v_mov_b32_e32 v54, 0
	v_mov_b32_e32 v55, 0
	s_mov_b32 s52, 0
	s_mov_b32 s53, 0
	s_cmp_lt_u32 s52, s39
	s_cbranch_scc0 .Lagg_slowdone_1
.Lagg_slowloop_1:
	s_load_dword s54, s[44:45], s53
	s_waitcnt lgkmcnt(0)
	s_bfe_u32 s64, s54, 0x70010
	s_bfe_u32 s65, s54, 0x10017
	s_mul_i32 s65, s65, 0x62
	s_add_u32 s64, s64, s65
	s_and_b32 s54, s54, 0xffff
	s_mul_i32 s54, s54, s46
	v_cmp_eq_u32_e32 vcc, s64, v2
	s_and_saveexec_b64 s[62:63], vcc
	s_cbranch_execz .Lagg_slownext_1
	v_add_u32_e32 v24, s54, v1
	global_load_dwordx4 v[28:31], v24, s[48:49] offset:64
	global_load_dwordx4 v[24:27], v24, s[48:49]
	v_mov_b32_e32 v56, v43
	s_waitcnt vmcnt(0)
	v_dot2c_f32_f16_e32 v56, v24, v16
	v_dot2c_f32_f16_e32 v56, v25, v17
	v_dot2c_f32_f16_e32 v56, v26, v18
	v_dot2c_f32_f16_e32 v56, v27, v19
	v_dot2c_f32_f16_e32 v56, v28, v20
	v_dot2c_f32_f16_e32 v56, v29, v21
	v_dot2c_f32_f16_e32 v56, v30, v22
	v_dot2c_f32_f16_e32 v56, v31, v23
	s_nop 2
	v_add_f32_dpp v56, v56, v56 quad_perm:[1,0,3,2] row_mask:0xf bank_mask:0xf bound_ctrl:1
	s_nop 0
	v_fmamk_f32 v58, v56, 0x3c23d70a, v44
	v_max_f32_e32 v56, v56, v58
	v_exp_f32_e32 v56, v56
	s_nop 0
	v_add_f32_e32 v45, v45, v56
	v_cvt_f16_f32_e32 v58, v56
	s_nop 0
	v_pk_fma_f16 v48, v24, v58, v48 op_sel_hi:[1,0,1]
	v_pk_fma_f16 v49, v25, v58, v49 op_sel_hi:[1,0,1]
	v_pk_fma_f16 v50, v26, v58, v50 op_sel_hi:[1,0,1]
	v_pk_fma_f16 v51, v27, v58, v51 op_sel_hi:[1,0,1]
	v_pk_fma_f16 v52, v28, v58, v52 op_sel_hi:[1,0,1]
	v_pk_fma_f16 v53, v29, v58, v53 op_sel_hi:[1,0,1]
	v_pk_fma_f16 v54, v30, v58, v54 op_sel_hi:[1,0,1]
	v_pk_fma_f16 v55, v31, v58, v55 op_sel_hi:[1,0,1]

	.amdhsa_kernel _Z10agg_kernelPKjPKiPKDF16_S4_PKfS4_S0_S2_S2_S2_S2_Pf
		.amdhsa_group_segment_fixed_size 77696
		.amdhsa_private_segment_fixed_size 0
		.amdhsa_kernarg_size 96
		.amdhsa_user_sgpr_count 2
		.amdhsa_user_sgpr_dispatch_ptr 0
		.amdhsa_user_sgpr_queue_ptr 0
		.amdhsa_user_sgpr_kernarg_segment_ptr 1
		.amdhsa_user_sgpr_dispatch_id 0
		.amdhsa_user_sgpr_kernarg_preload_length 0
		.amdhsa_user_sgpr_kernarg_preload_offset 0
		.amdhsa_user_sgpr_private_segment_size 0
		.amdhsa_uses_dynamic_stack 0
		.amdhsa_enable_private_segment 0
		.amdhsa_system_sgpr_workgroup_id_x 1
		.amdhsa_system_sgpr_workgroup_id_y 0
		.amdhsa_system_sgpr_workgroup_id_z 0
		.amdhsa_system_sgpr_workgroup_info 0
		.amdhsa_system_vgpr_workitem_id 0
		.amdhsa_next_free_vgpr 64
		.amdhsa_next_free_sgpr 72
		.amdhsa_accum_offset 64
		.amdhsa_reserve_vcc 1
		.amdhsa_float_round_mode_32 0
		.amdhsa_float_round_mode_16_64 0
		.amdhsa_float_denorm_mode_32 3
		.amdhsa_float_denorm_mode_16_64 3
		.amdhsa_dx10_clamp 1
		.amdhsa_ieee_mode 1
		.amdhsa_fp16_overflow 0
		.amdhsa_tg_split 0
		.amdhsa_exception_fp_ieee_invalid_op 0
		.amdhsa_exception_fp_denorm_src 0
		.amdhsa_exception_fp_ieee_div_zero 0
		.amdhsa_exception_fp_ieee_overflow 0
		.amdhsa_exception_fp_ieee_underflow 0
		.amdhsa_exception_fp_ieee_inexact 0
		.amdhsa_exception_int_div_zero 0
	.end_amdhsa_kernel

amdhsa.kernels:
  - .agpr_count:     0
    .args:
      - .actual_access:  read_only
        .address_space:  global
        .offset:         0
        .size:           8
        .value_kind:     global_buffer
      - .actual_access:  read_only
        .address_space:  global
        .offset:         8
        .size:           8
        .value_kind:     global_buffer
      - .actual_access:  read_only
        .address_space:  global
        .offset:         16
        .size:           8
        .value_kind:     global_buffer
      - .actual_access:  read_only
        .address_space:  global
        .offset:         24
        .size:           8
        .value_kind:     global_buffer
      - .actual_access:  read_only
        .address_space:  global
        .offset:         32
        .size:           8
        .value_kind:     global_buffer
      - .actual_access:  read_only
        .address_space:  global
        .offset:         40
        .size:           8
        .value_kind:     global_buffer
      - .actual_access:  read_only
        .address_space:  global
        .offset:         48
        .size:           8
        .value_kind:     global_buffer
      - .actual_access:  write_only
        .address_space:  global
        .offset:         56
        .size:           8
        .value_kind:     global_buffer
      - .actual_access:  write_only
        .address_space:  global
        .offset:         64
        .size:           8
        .value_kind:     global_buffer
      - .actual_access:  write_only
        .address_space:  global
        .offset:         72
        .size:           8
        .value_kind:     global_buffer
      - .actual_access:  write_only
        .address_space:  global
        .offset:         80
        .size:           8
        .value_kind:     global_buffer
      - .actual_access:  read_only
        .address_space:  global
        .offset:         88
        .size:           8
        .value_kind:     global_buffer
      - .actual_access:  read_only
        .address_space:  global
        .offset:         96
        .size:           8
        .value_kind:     global_buffer
      - .actual_access:  write_only
        .address_space:  global
        .offset:         104
        .size:           8
        .value_kind:     global_buffer
    .group_segment_fixed_size: 1024
    .kernarg_segment_align: 8
    .kernarg_segment_size: 112
    .language:       OpenCL C
    .language_version:
      - 2
      - 0
    .max_flat_workgroup_size: 1024
    .name:           _Z17prep_count_kernelPKfS0_S0_S0_S0_S0_S0_PDF16_PjPfS1_PKiS5_Pi
    .private_segment_fixed_size: 0
    .sgpr_count:     27
    .sgpr_spill_count: 0
    .symbol:         _Z17prep_count_kernelPKfS0_S0_S0_S0_S0_S0_PDF16_PjPfS1_PKiS5_Pi.kd
    .uniform_work_group_size: 1
    .uses_dynamic_stack: false
    .vgpr_count:     62
    .vgpr_spill_count: 0
    .wavefront_size: 64
  - .agpr_count:     0
    .args:
      - .actual_access:  read_only
        .address_space:  global
        .offset:         0
        .size:           8
        .value_kind:     global_buffer
      - .actual_access:  read_only
        .address_space:  global
        .offset:         8
        .size:           8
        .value_kind:     global_buffer
      - .actual_access:  read_only
        .address_space:  global
        .offset:         16
        .size:           8
        .value_kind:     global_buffer
      - .actual_access:  write_only
        .address_space:  global
        .offset:         24
        .size:           8
        .value_kind:     global_buffer
      - .actual_access:  write_only
        .address_space:  global
        .offset:         32
        .size:           8
        .value_kind:     global_buffer
      - .actual_access:  write_only
        .address_space:  global
        .offset:         40
        .size:           8
        .value_kind:     global_buffer
      - .address_space:  global
        .offset:         48
        .size:           8
        .value_kind:     global_buffer
      - .actual_access:  read_only
        .address_space:  global
        .offset:         56
        .size:           8
        .value_kind:     global_buffer
      - .actual_access:  read_only
        .address_space:  global
        .offset:         64
        .size:           8
        .value_kind:     global_buffer
      - .actual_access:  read_only
        .address_space:  global
        .offset:         72
        .size:           8
        .value_kind:     global_buffer
      - .actual_access:  read_only
        .address_space:  global
        .offset:         80
        .size:           8
        .value_kind:     global_buffer
      - .actual_access:  read_only
        .address_space:  global
        .offset:         88
        .size:           8
        .value_kind:     global_buffer
      - .actual_access:  write_only
        .address_space:  global
        .offset:         96
        .size:           8
        .value_kind:     global_buffer
      - .actual_access:  write_only
        .address_space:  global
        .offset:         104
        .size:           8
        .value_kind:     global_buffer
    .group_segment_fixed_size: 144320
    .kernarg_segment_align: 8
    .kernarg_segment_size: 112
    .language:       OpenCL C
    .language_version:
      - 2
      - 0
    .max_flat_workgroup_size: 512
    .name:           _Z19gemm_scatter_kernelPKfPKDF16_S0_PDF16_S3_PfPjPKiS7_S7_S7_S7_PiS5_
    .private_segment_fixed_size: 0
    .sgpr_count:     46
    .sgpr_spill_count: 0
    .symbol:         _Z19gemm_scatter_kernelPKfPKDF16_S0_PDF16_S3_PfPjPKiS7_S7_S7_S7_PiS5_.kd
    .uniform_work_group_size: 1
    .uses_dynamic_stack: false
    .vgpr_count:     230
    .vgpr_spill_count: 0
    .wavefront_size: 64
  - .agpr_count:     0
    .args:
      - .actual_access:  read_only
        .address_space:  global
        .offset:         0
        .size:           8
        .value_kind:     global_buffer
      - .actual_access:  read_only
        .address_space:  global
        .offset:         8
        .size:           8
        .value_kind:     global_buffer
      - .actual_access:  read_only
        .address_space:  global
        .offset:         16
        .size:           8
        .value_kind:     global_buffer
      - .actual_access:  read_only
        .address_space:  global
        .offset:         24
        .size:           8
        .value_kind:     global_buffer
      - .actual_access:  read_only
        .address_space:  global
        .offset:         32
        .size:           8
        .value_kind:     global_buffer
      - .actual_access:  read_only
        .address_space:  global
        .offset:         40
        .size:           8
        .value_kind:     global_buffer
      - .actual_access:  read_only
        .address_space:  global
        .offset:         48
        .size:           8
        .value_kind:     global_buffer
      - .actual_access:  read_only
        .address_space:  global
        .offset:         56
        .size:           8
        .value_kind:     global_buffer
      - .actual_access:  read_only
        .address_space:  global
        .offset:         64
        .size:           8
        .value_kind:     global_buffer
      - .actual_access:  read_only
        .address_space:  global
        .offset:         72
        .size:           8
        .value_kind:     global_buffer
      - .actual_access:  read_only
        .address_space:  global
        .offset:         80
        .size:           8
        .value_kind:     global_buffer
      - .actual_access:  write_only
        .address_space:  global
        .offset:         88
        .size:           8
        .value_kind:     global_buffer
    .group_segment_fixed_size: 77696
    .kernarg_segment_align: 8
    .kernarg_segment_size: 96
    .language:       OpenCL C
    .language_version:
      - 2
      - 0
    .max_flat_workgroup_size: 1024
    .name:           _Z10agg_kernelPKjPKiPKDF16_S4_PKfS4_S0_S2_S2_S2_S2_Pf
    .private_segment_fixed_size: 0
    .sgpr_count:     78
    .sgpr_spill_count: 0
    .symbol:         _Z10agg_kernelPKjPKiPKDF16_S4_PKfS4_S0_S2_S2_S2_S2_Pf.kd
    .uniform_work_group_size: 1
    .uses_dynamic_stack: false
    .vgpr_count:     64
    .vgpr_spill_count: 0
    .wavefront_size: 64
